# speedup vs baseline: 1.0366x; 1.0122x over previous
.LBB1_7:
	s_or_b64 exec, exec, s[2:3]
	v_mov_b32_e32 v10, v167
	s_waitcnt lgkmcnt(0)
	s_barrier
	s_waitcnt vmcnt(18)
	s_ashr_i32 s2, s4, 6
	s_lshl_b32 s3, s2, 3
	s_and_b32 s5, s3, 8
	s_bfe_u32 s26, s2, 0x10001
	s_or_b32 s5, s26, s5
	s_lshl_b32 s26, s2, 9
	s_and_b32 s26, s26, 0x400
	s_lshl_b32 s5, s5, 4
	s_or_b32 s28, s5, s26
	v_lshrrev_b32_e32 v182, 5, v167
	v_bfe_u32 v2, v156, 4, 1
	v_bitop3_b32 v3, v182, v156, 1 bitop3:0x78
	v_lshlrev_b32_e32 v154, 2, v182
	v_xor_b32_e32 v3, v3, v2
	v_bitop3_b32 v4, v154, v156, 4 bitop3:0x78
	v_and_b32_e32 v5, 10, v156
	v_or3_b32 v3, v5, v4, v3
	s_lshl_b32 s5, s2, 4
	v_lshlrev_b32_e32 v3, 4, v3
	s_lshl_b32 s3, s2, 13
	s_and_b32 s29, s5, 16
	v_lshlrev_b32_e32 v170, 8, v182
	v_lshl_or_b32 v171, v2, 10, v3
	s_or_b32 s26, s29, s3
	v_bitop3_b32 v179, v171, s26, v170 bitop3:0x36
	s_or_b32 s5, s26, 0x280
	v_bitop3_b32 v178, v171, s5, v170 bitop3:0x36
	s_or_b32 s30, s3, 0x800
	s_or_b32 s33, s3, 0x1000
	s_or_b32 s29, s29, 64
	s_or_b32 s34, s29, s33
	v_bitop3_b32 v180, v171, s34, v170 bitop3:0x36
	s_or_b32 s29, s3, s29
	s_or_b32 s29, s29, 0x1280
	s_and_b32 s5, s2, 1
	s_lshl_b32 s31, s5, 4
	s_or_b32 s2, s31, s3
	v_bitop3_b32 v173, v171, s2, v170 bitop3:0x36
	v_bitop3_b32 v34, v156, 31, v156 bitop3:0xc
	v_lshrrev_b32_e32 v35, 4, v34
	v_bitop3_b32 v36, v34, v182, 1 bitop3:0x6c
	v_xor_b32_e32 v36, v36, v35
	v_bitop3_b32 v34, v34, v154, 4 bitop3:0x6c
	v_bitop3_b32 v37, v156, 10, 31 bitop3:8
	v_or3_b32 v34, v37, v34, v36
	v_lshlrev_b32_e32 v35, 10, v35
	v_lshlrev_b32_e32 v34, 4, v34
	v_or3_b32 v154, v35, v34, v170
	v_bitop3_b32 v172, s2, v154, v159 bitop3:0x36
	v_bitop3_b32 v176, v171, s29, v170 bitop3:0x36
	s_or_b32 s29, s31, s30
	s_or_b32 s29, s29, 0xa0
	v_bitop3_b32 v175, v171, s29, v170 bitop3:0x36
	s_or_b32 s29, s2, 0xaa0
	s_xor_b32 s29, s29, 0x80
	v_xor_b32_e32 v174, s29, v154
	s_or_b32 s29, s26, 0x18e0
	v_bitop3_b32 v181, v171, s29, v170 bitop3:0x36
	s_or_b32 s29, s26, 0x1a60
	v_bitop3_b32 v177, v171, s29, v170 bitop3:0x36
	s_or_b32 s29, s31, 64
	s_or_b32 s3, s3, s29
	s_mov_b32 s41, s3
	s_or_b32 s29, s29, s33
	s_mov_b32 s40, s29
	s_or_b32 s3, s2, 0x18e0
	s_mov_b32 s42, s3
	s_or_b32 s2, s2, 0x1ae0
	s_xor_b32 s2, s2, 0x80
	s_mov_b32 s43, s2
	s_lshr_b32 s38, s4, 1
	v_and_b32_e32 v26, 31, v167
	v_and_b32_e32 v27, 3, v167
	v_bfe_u32 v28, v167, 3, 1
	v_bfe_u32 v29, v167, 2, 1
	v_lshl_or_b32 v27, v28, 2, v27
	v_lshl_or_b32 v27, v29, 3, v27
	v_lshlrev_b32_e32 v32, 9, v182
	v_lshl_add_u32 v30, v27, 3, v32
	v_add_u32_e32 v30, 0x10000, v30
	v_lshl_add_u32 v31, v26, 3, v32
	v_add_u32_e32 v31, 0x10400, v31
	v_xor_b32_e32 v28, 31, v26
	v_lshl_add_u32 v28, v28, 3, v32
	v_add_u32_e32 v28, 0x10400, v28
	v_bfe_u32 v29, v167, 4, 1
	v_mul_u32_u24_e32 v29, 0x78, v29
	v_xor_b32_e32 v254, s38, v29
	v_or_b32_e32 v254, 0x10800, v254
	v_and_b32_e32 v33, 16, v167
	v_cmp_eq_u32_e32 vcc, 0, v33
	ds_read2_b64 v[66:69], v30 offset0:0 offset1:32
	ds_read2_b64 v[70:73], v30 offset0:16 offset1:48
	ds_read2_b64 v[230:233], v31 offset0:0 offset1:32
	ds_read2_b64 v[234:237], v28 offset0:0 offset1:32
	ds_read2_b64 v[238:241], v254 offset0:0 offset1:16
	ds_read2_b64 v[242:245], v254 offset0:32 offset1:48
	s_waitcnt lgkmcnt(0)
	v_cndmask_b32_e32 v74, v67, v66, vcc
	v_cndmask_b32_e32 v75, v69, v68, vcc
	v_cndmask_b32_e64 v76, v66, -v67, vcc
	v_cndmask_b32_e64 v77, v68, -v69, vcc
	v_cndmask_b32_e32 v78, v71, v70, vcc
	v_cndmask_b32_e32 v79, v73, v72, vcc
	v_cndmask_b32_e64 v80, v70, -v71, vcc
	v_cndmask_b32_e64 v81, v72, -v73, vcc
	v_cvt_pk_f16_f32 v222, v74, v75
	v_cvt_pk_f16_f32 v223, v74, v75
	v_cvt_pk_f16_f32 v224, v76, v77
	v_cvt_pk_f16_f32 v225, v76, v77
	v_cvt_pk_f16_f32 v226, v78, v79
	v_cvt_pk_f16_f32 v227, v78, v79
	v_cvt_pk_f16_f32 v228, v80, v81
	v_cvt_pk_f16_f32 v229, v80, v81
	v_mul_f32_e32 v66, v231, v239
	v_mul_f32_e32 v68, v231, v238
	v_mul_f32_e32 v67, v231, v241
	v_mul_f32_e32 v69, v231, v240
	v_fma_f32 v66, v230, v238, -v66
	v_fma_f32 v68, v230, v239, v68
	v_fma_f32 v67, v230, v240, -v67
	v_fma_f32 v69, v230, v241, v69
	v_cvt_pk_f16_f32 v246, v66, v67
	v_cvt_pk_f16_f32 v248, v68, v69
	v_mul_f32_e32 v70, v233, v243
	v_mul_f32_e32 v72, v233, v242
	v_mul_f32_e32 v71, v233, v245
	v_mul_f32_e32 v73, v233, v244
	v_fma_f32 v70, v232, v242, -v70
	v_fma_f32 v72, v232, v243, v72
	v_fma_f32 v71, v232, v244, -v71
	v_fma_f32 v73, v232, v245, v73
	v_cvt_pk_f16_f32 v247, v70, v71
	v_cvt_pk_f16_f32 v249, v72, v73
	v_mul_f32_e32 v66, v235, v239
	v_mul_f32_e32 v68, v235, v238
	v_mul_f32_e32 v67, v235, v241
	v_mul_f32_e32 v69, v235, v240
	v_fma_f32 v66, v234, v238, -v66
	v_fma_f32 v68, v234, v239, v68
	v_fma_f32 v67, v234, v240, -v67
	v_fma_f32 v69, v234, v241, v69
	v_cvt_pk_f16_f32 v250, v66, v67
	v_cvt_pk_f16_f32 v252, v68, v69
	v_mul_f32_e32 v70, v237, v243
	v_mul_f32_e32 v72, v237, v242
	v_mul_f32_e32 v71, v237, v245
	v_mul_f32_e32 v73, v237, v244
	v_fma_f32 v70, v236, v242, -v70
	v_fma_f32 v72, v236, v243, v72
	v_fma_f32 v71, v236, v244, -v71
	v_fma_f32 v73, v236, v245, v73
	v_cvt_pk_f16_f32 v251, v70, v71
	v_cvt_pk_f16_f32 v253, v72, v73
	v_xor_b32_e32 v255, 8, v254
	ds_read2_b64 v[238:241], v255 offset0:0 offset1:16
	ds_read2_b64 v[242:245], v255 offset0:32 offset1:48
	v_mfma_f32_32x32x16_f16 v[2:17], v[222:225], v[246:249], 0
	v_mfma_f32_32x32x16_f16 v[18:33], v[226:229], v[250:253], 0
	s_waitcnt lgkmcnt(0)
	v_mul_f32_e32 v66, v231, v239
	v_mul_f32_e32 v68, v231, v238
	v_mul_f32_e32 v67, v231, v241
	v_mul_f32_e32 v69, v231, v240
	v_fma_f32 v66, v230, v238, -v66
	v_fma_f32 v68, v230, v239, v68
	v_fma_f32 v67, v230, v240, -v67
	v_fma_f32 v69, v230, v241, v69
	v_cvt_pk_f16_f32 v246, v66, v67
	v_cvt_pk_f16_f32 v248, v68, v69
	v_mul_f32_e32 v70, v233, v243
	v_mul_f32_e32 v72, v233, v242
	v_mul_f32_e32 v71, v233, v245
	v_mul_f32_e32 v73, v233, v244
	v_fma_f32 v70, v232, v242, -v70
	v_fma_f32 v72, v232, v243, v72
	v_fma_f32 v71, v232, v244, -v71
	v_fma_f32 v73, v232, v245, v73
	v_cvt_pk_f16_f32 v247, v70, v71
	v_cvt_pk_f16_f32 v249, v72, v73
	v_cvt_pk_f16_f32 v2, v2, v3
	v_cvt_pk_f16_f32 v3, v4, v5
	v_cvt_pk_f16_f32 v4, v6, v7
	v_cvt_pk_f16_f32 v5, v8, v9
	v_cvt_pk_f16_f32 v6, v10, v11
	v_cvt_pk_f16_f32 v7, v12, v13
	v_cvt_pk_f16_f32 v8, v14, v15
	v_cvt_pk_f16_f32 v9, v16, v17
	v_cvt_pk_f16_f32 v18, v18, v19
	v_cvt_pk_f16_f32 v19, v20, v21
	v_cvt_pk_f16_f32 v20, v22, v23
	v_cvt_pk_f16_f32 v21, v24, v25
	v_cvt_pk_f16_f32 v22, v26, v27
	v_cvt_pk_f16_f32 v23, v28, v29
	v_cvt_pk_f16_f32 v24, v30, v31
	v_cvt_pk_f16_f32 v25, v32, v33
	s_setprio 1
	s_waitcnt vmcnt(14)
	v_mul_f32_e32 v66, v235, v239
	v_mul_f32_e32 v68, v235, v238
	v_mfma_f32_32x32x16_f16 v[34:49], v[2:5], v[150:153], 0
	v_mul_f32_e32 v67, v235, v241
	v_mul_f32_e32 v69, v235, v240
	v_mfma_f32_32x32x16_f16 v[34:49], v[18:21], v[146:149], v[34:49]
	v_fma_f32 v66, v234, v238, -v66
	v_fma_f32 v68, v234, v239, v68
	v_mfma_f32_32x32x16_f16 v[34:49], v[6:9], v[142:145], v[34:49]
	v_fma_f32 v67, v234, v240, -v67
	v_fma_f32 v69, v234, v241, v69
	v_mfma_f32_32x32x16_f16 v[34:49], v[22:25], v[138:141], v[34:49]
	v_cvt_pk_f16_f32 v250, v66, v67
	v_cvt_pk_f16_f32 v252, v68, v69
	s_waitcnt vmcnt(5)
	v_mul_f32_e32 v70, v237, v243
	v_mul_f32_e32 v72, v237, v242
	v_mfma_f32_32x32x16_f16 v[50:65], v[2:5], v[134:137], 0
	v_mul_f32_e32 v71, v237, v245
	v_mul_f32_e32 v73, v237, v244
	v_mfma_f32_32x32x16_f16 v[50:65], v[18:21], v[126:129], v[50:65]
	v_fma_f32 v70, v236, v242, -v70
	v_fma_f32 v72, v236, v243, v72
	v_mfma_f32_32x32x16_f16 v[50:65], v[6:9], v[122:125], v[50:65]
	v_fma_f32 v71, v236, v244, -v71
	v_fma_f32 v73, v236, v245, v73
	v_mfma_f32_32x32x16_f16 v[50:65], v[22:25], v[130:133], v[50:65]
	v_cvt_pk_f16_f32 v251, v70, v71
	v_cvt_pk_f16_f32 v253, v72, v73
	v_xor_b32_e32 v255, 16, v254
	ds_read2_b64 v[238:241], v255 offset0:0 offset1:16
	ds_read2_b64 v[242:245], v255 offset0:32 offset1:48
	v_mfma_f32_32x32x16_f16 v[2:17], v[222:225], v[246:249], 0
	v_mfma_f32_32x32x16_f16 v[18:33], v[226:229], v[250:253], 0
	v_cvt_pk_f16_f32 v34, v34, v35
	v_cvt_pk_f16_f32 v35, v36, v37
	v_cvt_pk_f16_f32 v36, v38, v39
	v_cvt_pk_f16_f32 v37, v40, v41
	v_cvt_pk_f16_f32 v38, v42, v43
	v_cvt_pk_f16_f32 v39, v44, v45
	v_cvt_pk_f16_f32 v40, v46, v47
	v_cvt_pk_f16_f32 v41, v48, v49
	v_cvt_pk_f16_f32 v50, v50, v51
	v_cvt_pk_f16_f32 v51, v52, v53
	v_cvt_pk_f16_f32 v52, v54, v55
	v_cvt_pk_f16_f32 v53, v56, v57
	v_cvt_pk_f16_f32 v54, v58, v59
	v_cvt_pk_f16_f32 v55, v60, v61
	v_cvt_pk_f16_f32 v56, v62, v63
	v_cvt_pk_f16_f32 v57, v64, v65
	s_waitcnt vmcnt(2)
	v_cvt_pk_f16_f32 v2, v2, v3
	v_cvt_pk_f16_f32 v3, v4, v5
	v_cvt_pk_f16_f32 v4, v6, v7
	v_cvt_pk_f16_f32 v5, v8, v9
	v_mfma_f32_32x32x16_f16 v[190:205], v[34:37], v[118:121], 0
	v_cvt_pk_f16_f32 v6, v10, v11
	v_cvt_pk_f16_f32 v7, v12, v13
	v_cvt_pk_f16_f32 v8, v14, v15
	v_cvt_pk_f16_f32 v9, v16, v17
	v_mfma_f32_32x32x16_f16 v[206:221], v[34:37], v[102:105], 0
	v_cvt_pk_f16_f32 v18, v18, v19
	v_cvt_pk_f16_f32 v19, v20, v21
	v_cvt_pk_f16_f32 v20, v22, v23
	v_cvt_pk_f16_f32 v21, v24, v25
	v_mfma_f32_32x32x16_f16 v[190:205], v[38:41], v[114:117], v[190:205]
	v_cvt_pk_f16_f32 v22, v26, v27
	v_cvt_pk_f16_f32 v23, v28, v29
	v_cvt_pk_f16_f32 v24, v30, v31
	v_cvt_pk_f16_f32 v25, v32, v33
	v_mfma_f32_32x32x16_f16 v[206:221], v[38:41], v[98:101], v[206:221]
	s_waitcnt lgkmcnt(0)
	v_mul_f32_e32 v66, v231, v239
	v_mul_f32_e32 v68, v231, v238
	v_mul_f32_e32 v67, v231, v241
	v_mfma_f32_32x32x16_f16 v[190:205], v[50:53], v[110:113], v[190:205]
	v_mul_f32_e32 v69, v231, v240
	v_fma_f32 v66, v230, v238, -v66
	v_fma_f32 v68, v230, v239, v68
	v_fma_f32 v67, v230, v240, -v67
	v_mfma_f32_32x32x16_f16 v[206:221], v[50:53], v[94:97], v[206:221]
	v_fma_f32 v69, v230, v241, v69
	v_cvt_pk_f16_f32 v246, v66, v67
	v_cvt_pk_f16_f32 v248, v68, v69
	v_mul_f32_e32 v70, v233, v243
	v_mfma_f32_32x32x16_f16 v[190:205], v[54:57], v[106:109], v[190:205]
	v_mul_f32_e32 v72, v233, v242
	v_mul_f32_e32 v71, v233, v245
	v_mul_f32_e32 v73, v233, v244
	v_fma_f32 v70, v232, v242, -v70
	v_mfma_f32_32x32x16_f16 v[206:221], v[54:57], v[90:93], v[206:221]
	v_fma_f32 v72, v232, v243, v72
	v_fma_f32 v71, v232, v244, -v71
	v_fma_f32 v73, v232, v245, v73
	v_cvt_pk_f16_f32 v247, v70, v71
	v_cvt_pk_f16_f32 v249, v72, v73
	v_mfma_f32_32x32x16_f16 v[34:49], v[2:5], v[150:153], 0
	v_mul_f32_e32 v66, v235, v239
	v_mul_f32_e32 v68, v235, v238
	v_mul_f32_e32 v67, v235, v241
	v_mul_f32_e32 v69, v235, v240
	v_fma_f32 v66, v234, v238, -v66
	v_mfma_f32_32x32x16_f16 v[34:49], v[18:21], v[146:149], v[34:49]
	v_fma_f32 v68, v234, v239, v68
	v_fma_f32 v67, v234, v240, -v67
	v_fma_f32 v69, v234, v241, v69
	v_cvt_pk_f16_f32 v250, v66, v67
	v_cvt_pk_f16_f32 v252, v68, v69
	v_mfma_f32_32x32x16_f16 v[34:49], v[6:9], v[142:145], v[34:49]
	v_mul_f32_e32 v70, v237, v243
	v_mul_f32_e32 v72, v237, v242
	v_mul_f32_e32 v71, v237, v245
	v_mul_f32_e32 v73, v237, v244
	v_fma_f32 v70, v236, v242, -v70
	v_mfma_f32_32x32x16_f16 v[34:49], v[22:25], v[138:141], v[34:49]
	v_fma_f32 v72, v236, v243, v72
	v_fma_f32 v71, v236, v244, -v71
	v_fma_f32 v73, v236, v245, v73
	v_cvt_pk_f16_f32 v251, v70, v71
	v_cvt_pk_f16_f32 v253, v72, v73
	v_mfma_f32_32x32x16_f16 v[50:65], v[2:5], v[134:137], 0
	v_cvt_pk_f16_f32 v190, v190, v191
	v_cvt_pk_f16_f32 v191, v192, v193
	v_cvt_pk_f16_f32 v192, v194, v195
	v_cvt_pk_f16_f32 v193, v196, v197
	v_cvt_pk_f16_f32 v194, v198, v199
	v_mfma_f32_32x32x16_f16 v[50:65], v[18:21], v[126:129], v[50:65]
	v_cvt_pk_f16_f32 v195, v200, v201
	v_cvt_pk_f16_f32 v196, v202, v203
	v_cvt_pk_f16_f32 v197, v204, v205
	v_cvt_pk_f16_f32 v206, v206, v207
	v_cvt_pk_f16_f32 v207, v208, v209
	v_mfma_f32_32x32x16_f16 v[50:65], v[6:9], v[122:125], v[50:65]
	v_cvt_pk_f16_f32 v208, v210, v211
	v_cvt_pk_f16_f32 v209, v212, v213
	v_cvt_pk_f16_f32 v210, v214, v215
	v_cvt_pk_f16_f32 v211, v216, v217
	v_cvt_pk_f16_f32 v212, v218, v219
	v_mfma_f32_32x32x16_f16 v[50:65], v[22:25], v[130:133], v[50:65]
	v_cvt_pk_f16_f32 v213, v220, v221
	ds_write_b128 v173, v[190:193]
	ds_write_b128 v172, v[194:197]
	ds_write_b128 v173, v[206:209] offset:32768
	ds_write_b128 v172, v[210:213] offset:32768
	v_xor_b32_e32 v255, 24, v254
	ds_read2_b64 v[238:241], v255 offset0:0 offset1:16
	ds_read2_b64 v[242:245], v255 offset0:32 offset1:48
	v_mfma_f32_32x32x16_f16 v[2:17], v[222:225], v[246:249], 0
	v_mfma_f32_32x32x16_f16 v[18:33], v[226:229], v[250:253], 0
	v_cvt_pk_f16_f32 v34, v34, v35
	v_cvt_pk_f16_f32 v35, v36, v37
	v_cvt_pk_f16_f32 v36, v38, v39
	v_cvt_pk_f16_f32 v37, v40, v41
	v_cvt_pk_f16_f32 v38, v42, v43
	v_cvt_pk_f16_f32 v39, v44, v45
	v_cvt_pk_f16_f32 v40, v46, v47
	v_cvt_pk_f16_f32 v41, v48, v49
	v_cvt_pk_f16_f32 v50, v50, v51
	v_cvt_pk_f16_f32 v51, v52, v53
	v_cvt_pk_f16_f32 v52, v54, v55
	v_cvt_pk_f16_f32 v53, v56, v57
	v_cvt_pk_f16_f32 v54, v58, v59
	v_cvt_pk_f16_f32 v55, v60, v61
	v_cvt_pk_f16_f32 v56, v62, v63
	v_cvt_pk_f16_f32 v57, v64, v65
	v_mfma_f32_32x32x16_f16 v[190:205], v[34:37], v[118:121], 0
	v_cvt_pk_f16_f32 v2, v2, v3
	v_cvt_pk_f16_f32 v3, v4, v5
	v_cvt_pk_f16_f32 v4, v6, v7
	v_cvt_pk_f16_f32 v5, v8, v9
	v_mfma_f32_32x32x16_f16 v[206:221], v[34:37], v[102:105], 0
	v_cvt_pk_f16_f32 v6, v10, v11
	v_cvt_pk_f16_f32 v7, v12, v13
	v_cvt_pk_f16_f32 v8, v14, v15
	v_cvt_pk_f16_f32 v9, v16, v17
	v_cvt_pk_f16_f32 v18, v18, v19
	v_mfma_f32_32x32x16_f16 v[190:205], v[38:41], v[114:117], v[190:205]
	v_cvt_pk_f16_f32 v19, v20, v21
	v_cvt_pk_f16_f32 v20, v22, v23
	v_cvt_pk_f16_f32 v21, v24, v25
	v_cvt_pk_f16_f32 v22, v26, v27
	v_mfma_f32_32x32x16_f16 v[206:221], v[38:41], v[98:101], v[206:221]
	v_cvt_pk_f16_f32 v23, v28, v29
	v_cvt_pk_f16_f32 v24, v30, v31
	v_cvt_pk_f16_f32 v25, v32, v33
	s_waitcnt lgkmcnt(0)
	v_mul_f32_e32 v66, v231, v239
	v_mfma_f32_32x32x16_f16 v[190:205], v[50:53], v[110:113], v[190:205]
	v_mul_f32_e32 v68, v231, v238
	v_mul_f32_e32 v67, v231, v241
	v_mul_f32_e32 v69, v231, v240
	v_fma_f32 v66, v230, v238, -v66
	v_fma_f32 v68, v230, v239, v68
	v_mfma_f32_32x32x16_f16 v[206:221], v[50:53], v[94:97], v[206:221]
	v_fma_f32 v67, v230, v240, -v67
	v_fma_f32 v69, v230, v241, v69
	v_cvt_pk_f16_f32 v246, v66, v67
	v_cvt_pk_f16_f32 v248, v68, v69
	v_mfma_f32_32x32x16_f16 v[190:205], v[54:57], v[106:109], v[190:205]
	v_mul_f32_e32 v70, v233, v243
	v_mul_f32_e32 v72, v233, v242
	v_mul_f32_e32 v71, v233, v245
	v_mul_f32_e32 v73, v233, v244
	v_fma_f32 v70, v232, v242, -v70
	v_mfma_f32_32x32x16_f16 v[206:221], v[54:57], v[90:93], v[206:221]
	v_fma_f32 v72, v232, v243, v72
	v_fma_f32 v71, v232, v244, -v71
	v_fma_f32 v73, v232, v245, v73
	v_cvt_pk_f16_f32 v247, v70, v71
	v_cvt_pk_f16_f32 v249, v72, v73
	v_mfma_f32_32x32x16_f16 v[34:49], v[2:5], v[150:153], 0
	v_mul_f32_e32 v66, v235, v239
	v_mul_f32_e32 v68, v235, v238
	v_mul_f32_e32 v67, v235, v241
	v_mul_f32_e32 v69, v235, v240
	v_fma_f32 v66, v234, v238, -v66
	v_mfma_f32_32x32x16_f16 v[34:49], v[18:21], v[146:149], v[34:49]
	v_fma_f32 v68, v234, v239, v68
	v_fma_f32 v67, v234, v240, -v67
	v_fma_f32 v69, v234, v241, v69
	v_cvt_pk_f16_f32 v250, v66, v67
	v_cvt_pk_f16_f32 v252, v68, v69
	v_mfma_f32_32x32x16_f16 v[34:49], v[6:9], v[142:145], v[34:49]
	v_mul_f32_e32 v70, v237, v243
	v_mul_f32_e32 v72, v237, v242
	v_mul_f32_e32 v71, v237, v245
	v_mul_f32_e32 v73, v237, v244
	v_fma_f32 v70, v236, v242, -v70
	v_mfma_f32_32x32x16_f16 v[34:49], v[22:25], v[138:141], v[34:49]
	v_fma_f32 v72, v236, v243, v72
	v_fma_f32 v71, v236, v244, -v71
	v_fma_f32 v73, v236, v245, v73
	v_cvt_pk_f16_f32 v251, v70, v71
	v_cvt_pk_f16_f32 v253, v72, v73
	v_cvt_pk_f16_f32 v190, v190, v191
	v_mfma_f32_32x32x16_f16 v[50:65], v[2:5], v[134:137], 0
	v_cvt_pk_f16_f32 v191, v192, v193
	v_cvt_pk_f16_f32 v192, v194, v195
	v_cvt_pk_f16_f32 v193, v196, v197
	v_cvt_pk_f16_f32 v194, v198, v199
	v_cvt_pk_f16_f32 v195, v200, v201
	v_mfma_f32_32x32x16_f16 v[50:65], v[18:21], v[126:129], v[50:65]
	v_cvt_pk_f16_f32 v196, v202, v203
	v_cvt_pk_f16_f32 v197, v204, v205
	v_cvt_pk_f16_f32 v206, v206, v207
	v_cvt_pk_f16_f32 v207, v208, v209
	v_cvt_pk_f16_f32 v208, v210, v211
	v_mfma_f32_32x32x16_f16 v[50:65], v[6:9], v[122:125], v[50:65]
	v_cvt_pk_f16_f32 v209, v212, v213
	v_cvt_pk_f16_f32 v210, v214, v215
	v_cvt_pk_f16_f32 v211, v216, v217
	v_cvt_pk_f16_f32 v212, v218, v219
	v_cvt_pk_f16_f32 v213, v220, v221
	v_mfma_f32_32x32x16_f16 v[50:65], v[22:25], v[130:133], v[50:65]
	v_xor_b32_e32 v74, 0x8a0, v173
	v_xor_b32_e32 v75, 0x8a0, v172
	ds_write_b128 v74, v[190:193]
	ds_write_b128 v75, v[194:197]
	ds_write_b128 v74, v[206:209] offset:32768
	ds_write_b128 v75, v[210:213] offset:32768
	s_nop 0
	v_mfma_f32_32x32x16_f16 v[2:17], v[222:225], v[246:249], 0
	v_mfma_f32_32x32x16_f16 v[18:33], v[226:229], v[250:253], 0
	v_cvt_pk_f16_f32 v34, v34, v35
	v_cvt_pk_f16_f32 v35, v36, v37
	v_cvt_pk_f16_f32 v36, v38, v39
	v_cvt_pk_f16_f32 v37, v40, v41
	v_cvt_pk_f16_f32 v38, v42, v43
	v_cvt_pk_f16_f32 v39, v44, v45
	v_cvt_pk_f16_f32 v40, v46, v47
	v_cvt_pk_f16_f32 v41, v48, v49
	v_cvt_pk_f16_f32 v50, v50, v51
	v_cvt_pk_f16_f32 v51, v52, v53
	v_cvt_pk_f16_f32 v52, v54, v55
	v_cvt_pk_f16_f32 v53, v56, v57
	v_cvt_pk_f16_f32 v54, v58, v59
	v_cvt_pk_f16_f32 v55, v60, v61
	v_cvt_pk_f16_f32 v56, v62, v63
	v_cvt_pk_f16_f32 v57, v64, v65
	v_mfma_f32_32x32x16_f16 v[190:205], v[34:37], v[118:121], 0
	v_cvt_pk_f16_f32 v2, v2, v3
	v_cvt_pk_f16_f32 v3, v4, v5
	v_mfma_f32_32x32x16_f16 v[206:221], v[34:37], v[102:105], 0
	v_cvt_pk_f16_f32 v4, v6, v7
	v_cvt_pk_f16_f32 v5, v8, v9
	v_mfma_f32_32x32x16_f16 v[190:205], v[38:41], v[114:117], v[190:205]
	v_cvt_pk_f16_f32 v6, v10, v11
	v_cvt_pk_f16_f32 v7, v12, v13
	v_mfma_f32_32x32x16_f16 v[206:221], v[38:41], v[98:101], v[206:221]
	v_cvt_pk_f16_f32 v8, v14, v15
	v_cvt_pk_f16_f32 v9, v16, v17
	v_mfma_f32_32x32x16_f16 v[190:205], v[50:53], v[110:113], v[190:205]
	v_cvt_pk_f16_f32 v18, v18, v19
	v_cvt_pk_f16_f32 v19, v20, v21
	v_mfma_f32_32x32x16_f16 v[206:221], v[50:53], v[94:97], v[206:221]
	v_cvt_pk_f16_f32 v20, v22, v23
	v_cvt_pk_f16_f32 v21, v24, v25
	v_mfma_f32_32x32x16_f16 v[190:205], v[54:57], v[106:109], v[190:205]
	v_cvt_pk_f16_f32 v22, v26, v27
	v_cvt_pk_f16_f32 v23, v28, v29
	v_mfma_f32_32x32x16_f16 v[206:221], v[54:57], v[90:93], v[206:221]
	v_cvt_pk_f16_f32 v24, v30, v31
	v_cvt_pk_f16_f32 v25, v32, v33
	v_mfma_f32_32x32x16_f16 v[34:49], v[2:5], v[150:153], 0
	v_mfma_f32_32x32x16_f16 v[34:49], v[18:21], v[146:149], v[34:49]
	v_mfma_f32_32x32x16_f16 v[34:49], v[6:9], v[142:145], v[34:49]
	v_mfma_f32_32x32x16_f16 v[34:49], v[22:25], v[138:141], v[34:49]
	v_mfma_f32_32x32x16_f16 v[50:65], v[2:5], v[134:137], 0
	s_nop 5
	v_cvt_pk_f16_f32 v190, v190, v191
	v_cvt_pk_f16_f32 v191, v192, v193
	v_cvt_pk_f16_f32 v192, v194, v195
	v_cvt_pk_f16_f32 v193, v196, v197
	v_mfma_f32_32x32x16_f16 v[50:65], v[18:21], v[126:129], v[50:65]
	v_cvt_pk_f16_f32 v194, v198, v199
	v_cvt_pk_f16_f32 v195, v200, v201
	v_cvt_pk_f16_f32 v196, v202, v203
	v_cvt_pk_f16_f32 v197, v204, v205
	v_cvt_pk_f16_f32 v206, v206, v207
	v_cvt_pk_f16_f32 v207, v208, v209
	v_mfma_f32_32x32x16_f16 v[50:65], v[6:9], v[122:125], v[50:65]
	v_cvt_pk_f16_f32 v208, v210, v211
	v_cvt_pk_f16_f32 v209, v212, v213
	v_cvt_pk_f16_f32 v210, v214, v215
	v_cvt_pk_f16_f32 v211, v216, v217
	v_cvt_pk_f16_f32 v212, v218, v219
	v_cvt_pk_f16_f32 v213, v220, v221
	v_mfma_f32_32x32x16_f16 v[50:65], v[22:25], v[130:133], v[50:65]
	v_xor_b32_e32 v74, 0x1040, v173
	v_xor_b32_e32 v75, 0x1040, v172
	ds_write_b128 v74, v[190:193]
	ds_write_b128 v75, v[194:197]
	ds_write_b128 v74, v[206:209] offset:32768
	ds_write_b128 v75, v[210:213] offset:32768
	s_nop 11
	v_cvt_pk_f16_f32 v34, v34, v35
	v_cvt_pk_f16_f32 v35, v36, v37
	v_cvt_pk_f16_f32 v36, v38, v39
	v_cvt_pk_f16_f32 v37, v40, v41
	v_cvt_pk_f16_f32 v38, v42, v43
	v_cvt_pk_f16_f32 v39, v44, v45
	v_cvt_pk_f16_f32 v40, v46, v47
	v_cvt_pk_f16_f32 v41, v48, v49
	v_cvt_pk_f16_f32 v50, v50, v51
	v_cvt_pk_f16_f32 v51, v52, v53
	v_cvt_pk_f16_f32 v52, v54, v55
	v_cvt_pk_f16_f32 v53, v56, v57
	v_cvt_pk_f16_f32 v54, v58, v59
	v_cvt_pk_f16_f32 v55, v60, v61
	v_cvt_pk_f16_f32 v56, v62, v63
	v_cvt_pk_f16_f32 v57, v64, v65
	v_mfma_f32_32x32x16_f16 v[190:205], v[34:37], v[118:121], 0
	v_mfma_f32_32x32x16_f16 v[206:221], v[34:37], v[102:105], 0
	v_mfma_f32_32x32x16_f16 v[190:205], v[38:41], v[114:117], v[190:205]
	v_mfma_f32_32x32x16_f16 v[206:221], v[38:41], v[98:101], v[206:221]
	v_mfma_f32_32x32x16_f16 v[190:205], v[50:53], v[110:113], v[190:205]
	v_mfma_f32_32x32x16_f16 v[206:221], v[50:53], v[94:97], v[206:221]
	v_mfma_f32_32x32x16_f16 v[190:205], v[54:57], v[106:109], v[190:205]
	v_mfma_f32_32x32x16_f16 v[206:221], v[54:57], v[90:93], v[206:221]
	v_and_b32_e32 v134, 1, v156
	v_bitop3_b32 v132, v171, s40, v170 bitop3:0x36
	v_bitop3_b32 v131, s41, v154, v160 bitop3:0x36
	v_bitop3_b32 v135, v171, s42, v170 bitop3:0x36
	v_xor_b32_e32 v133, s43, v154
	v_and_b32_e32 v130, 4, v156
	s_lshl_b32 s2, s27, 3
	s_lshl_b32 s3, s5, 2
	s_or_b32 s2, s3, s2
	s_ashr_i32 s3, s2, 31
	s_lshl_b64 s[2:3], s[2:3], 13
	s_add_u32 s2, s20, s2
	s_addc_u32 s3, s21, s3
	v_lshlrev_b32_e32 v154, 1, v169
	v_lshl_add_u64 v[2:3], s[2:3], 0, v[154:155]
	v_add_co_u32_e32 v2, vcc, s23, v2
	s_nop 1
	v_addc_co_u32_e32 v3, vcc, 0, v3, vcc
	v_cvt_pk_f16_f32 v190, v190, v191
	v_cvt_pk_f16_f32 v191, v192, v193
	v_cvt_pk_f16_f32 v192, v194, v195
	v_cvt_pk_f16_f32 v193, v196, v197
	v_cvt_pk_f16_f32 v194, v198, v199
	v_cvt_pk_f16_f32 v195, v200, v201
	v_cvt_pk_f16_f32 v196, v202, v203
	v_cvt_pk_f16_f32 v197, v204, v205
	v_cvt_pk_f16_f32 v206, v206, v207
	v_cvt_pk_f16_f32 v207, v208, v209
	v_cvt_pk_f16_f32 v208, v210, v211
	v_cvt_pk_f16_f32 v209, v212, v213
	v_cvt_pk_f16_f32 v210, v214, v215
	v_cvt_pk_f16_f32 v211, v216, v217
	v_cvt_pk_f16_f32 v212, v218, v219
	v_cvt_pk_f16_f32 v213, v220, v221
	v_xor_b32_e32 v74, 0x18e0, v173
	v_xor_b32_e32 v75, 0x18e0, v172
	ds_write_b128 v74, v[190:193]
	ds_write_b128 v75, v[194:197]
	ds_write_b128 v74, v[206:209] offset:32768
	ds_write_b128 v75, v[210:213] offset:32768
	s_setprio 0
	s_waitcnt lgkmcnt(0)
	s_barrier
	global_load_dwordx4 v[62:65], v154, s[2:3]
	global_load_dwordx4 v[46:49], v154, s[2:3] offset:1024
	global_load_dwordx4 v[42:45], v154, s[2:3] offset:2048
	global_load_dwordx4 v[38:41], v154, s[2:3] offset:3072
	global_load_dwordx4 v[54:57], v[2:3], off offset:1024
	global_load_dwordx4 v[50:53], v[2:3], off offset:2048
	v_lshl_add_u64 v[4:5], s[12:13], 0, v[154:155]
	global_load_dwordx4 v[126:129], v154, s[12:13]
	global_load_dwordx4 v[122:125], v154, s[12:13] offset:1024
	global_load_dwordx4 v[118:121], v154, s[12:13] offset:2048
	global_load_dwordx4 v[114:117], v154, s[12:13] offset:3072
	global_load_dwordx4 v[34:37], v168, s[2:3]
	global_load_dwordx4 v[110:113], v168, s[12:13]
	v_add_co_u32_e32 v4, vcc, s23, v4
	s_nop 1
	v_addc_co_u32_e32 v5, vcc, 0, v5, vcc
	global_load_dwordx4 v[58:61], v[2:3], off offset:3072
	global_load_dwordx4 v[106:109], v[4:5], off offset:1024
	global_load_dwordx4 v[94:97], v[4:5], off offset:2048
	global_load_dwordx4 v[90:93], v[4:5], off offset:3072
	v_bfrev_b32_e32 v3, v156
	v_lshlrev_b32_e32 v7, 5, v167
	v_lshlrev_b32_e32 v6, 9, v167
	v_and_b32_e32 v7, 0x200, v7
	v_lshlrev_b32_e32 v8, 8, v167
	v_lshrrev_b32_e32 v3, 27, v3
	v_lshrrev_b32_e32 v2, 2, v167
	v_lshrrev_b32_e32 v4, 4, v156
	v_xor_b32_e32 v5, v169, v156
	v_and_b32_e32 v6, 0x5800, v6
	v_and_b32_e32 v3, 8, v3
	v_and_or_b32 v7, v8, s24, v7
	v_lshrrev_b32_e32 v5, 1, v5
	v_xor_b32_e32 v4, v2, v4
	v_or3_b32 v3, v7, v6, v3
	v_bitop3_b32 v7, v2, v182, 1 bitop3:0x6c
	v_lshlrev_b32_e32 v2, 1, v167
	v_and_b32_e32 v5, 4, v5
	v_lshlrev_b32_e32 v4, 3, v4
	v_lshrrev_b32_e32 v6, 1, v167
	v_and_b32_e32 v2, 2, v2
	v_and_or_b32 v9, v169, 8, v2
	v_and_b32_e32 v2, 8, v4
	v_and_or_b32 v4, v6, 2, v5
	v_or3_b32 v2, v4, v2, v134
	v_lshlrev_b32_e32 v2, 4, v2
	v_bitop3_b32 v146, v3, s28, v2 bitop3:0x36
	v_xor_b32_e32 v8, v6, v182
	v_xor_b32_e32 v147, 0x2010, v146
	v_lshlrev_b32_e32 v8, 2, v8
	v_and_b32_e32 v8, 4, v8
	v_or3_b32 v6, v9, v7, v8
	v_lshlrev_b32_e32 v7, 11, v167
	v_and_b32_e32 v8, 0x7800, v7
	v_lshlrev_b32_e32 v6, 4, v6
	v_or3_b32 v22, v6, v8, v170
	v_and_b32_e32 v23, 0x8000, v7
	v_xor_b32_e32 v150, 16, v146
	v_xad_u32 v70, v22, s28, v23
	v_xor_b32_e32 v151, 0x2000, v146
	ds_read_b64_tr_b16 v[18:19], v146
	ds_read_b64_tr_b16 v[20:21], v147
	ds_read_b64_tr_b16 v[22:23], v146 offset:32768
	ds_read_b64_tr_b16 v[24:25], v147 offset:32768
	ds_read_b64_tr_b16 v[26:27], v150
	ds_read_b64_tr_b16 v[28:29], v151
	ds_read_b64_tr_b16 v[30:31], v150 offset:32768
	ds_read_b64_tr_b16 v[32:33], v151 offset:32768
	v_xor_b32_e32 v148, 32, v146
	v_xor_b32_e32 v149, 0x2030, v146
	v_xor_b32_e32 v144, 48, v146
	v_xor_b32_e32 v145, 0x2020, v146
	v_xor_b32_e32 v142, 64, v146
	v_xor_b32_e32 v143, 0x2050, v146
	v_xor_b32_e32 v140, 0x50, v146
	v_xor_b32_e32 v141, 0x2040, v146
	v_xor_b32_e32 v138, 0x60, v146
	v_xor_b32_e32 v139, 0x2070, v146
	v_xor_b32_e32 v136, 0x70, v146
	v_xor_b32_e32 v137, 0x2060, v146
	v_xor_b32_e32 v71, 0x60, v70
	s_lshl_b64 s[0:1], s[0:1], 13
	s_add_u32 s0, s8, s0
	s_addc_u32 s1, s9, s1
	s_waitcnt vmcnt(17) lgkmcnt(4)
	v_mfma_f32_32x32x16_f16 v[2:17], v[18:21], v[86:89], 0
	s_waitcnt vmcnt(16)
	v_mfma_f32_32x32x16_f16 v[2:17], v[22:25], v[82:85], v[2:17]
	ds_read_b64_tr_b16 v[206:207], v148
	ds_read_b64_tr_b16 v[208:209], v149
	ds_read_b64_tr_b16 v[210:211], v148 offset:32768
	ds_read_b64_tr_b16 v[212:213], v149 offset:32768
	s_waitcnt lgkmcnt(4)
	v_mfma_f32_32x32x16_f16 v[190:205], v[26:29], v[86:89], 0
	v_mfma_f32_32x32x16_f16 v[190:205], v[30:33], v[82:85], v[190:205]
	s_nop 4
	v_cvt_pk_f16_f32 v2, v2, v3
	v_cvt_pk_f16_f32 v3, v4, v5
	v_cvt_pk_f16_f32 v4, v6, v7
	v_cvt_pk_f16_f32 v5, v8, v9
	v_cvt_pk_f16_f32 v6, v10, v11
	v_cvt_pk_f16_f32 v7, v12, v13
	v_cvt_pk_f16_f32 v8, v14, v15
	v_cvt_pk_f16_f32 v9, v16, v17
	v_xor_b32_e32 v73, 0x280, v70
	ds_write_b128 v70, v[2:5]
	ds_write_b128 v73, v[6:9]
	ds_read_b64_tr_b16 v[18:19], v144
	ds_read_b64_tr_b16 v[20:21], v145
	ds_read_b64_tr_b16 v[22:23], v144 offset:32768
	ds_read_b64_tr_b16 v[24:25], v145 offset:32768
	s_waitcnt lgkmcnt(6)
	v_mfma_f32_32x32x16_f16 v[2:17], v[206:209], v[86:89], 0
	v_mfma_f32_32x32x16_f16 v[2:17], v[210:213], v[82:85], v[2:17]
	v_cvt_pk_f16_f32 v190, v190, v191
	v_cvt_pk_f16_f32 v191, v192, v193
	v_cvt_pk_f16_f32 v192, v194, v195
	v_cvt_pk_f16_f32 v193, v196, v197
	v_cvt_pk_f16_f32 v194, v198, v199
	v_cvt_pk_f16_f32 v195, v200, v201
	v_cvt_pk_f16_f32 v196, v202, v203
	v_cvt_pk_f16_f32 v197, v204, v205
	v_xor_b32_e32 v72, 16, v70
	v_xor_b32_e32 v73, 0x290, v70
	ds_write_b128 v72, v[190:193]
	ds_write_b128 v73, v[194:197]
	ds_read_b64_tr_b16 v[26:27], v142
	ds_read_b64_tr_b16 v[28:29], v143
	ds_read_b64_tr_b16 v[30:31], v142 offset:32768
	ds_read_b64_tr_b16 v[32:33], v143 offset:32768
	s_waitcnt lgkmcnt(6)
	v_mfma_f32_32x32x16_f16 v[190:205], v[18:21], v[86:89], 0
	v_mfma_f32_32x32x16_f16 v[190:205], v[22:25], v[82:85], v[190:205]
	v_cvt_pk_f16_f32 v2, v2, v3
	v_cvt_pk_f16_f32 v3, v4, v5
	v_cvt_pk_f16_f32 v4, v6, v7
	v_cvt_pk_f16_f32 v5, v8, v9
	v_cvt_pk_f16_f32 v6, v10, v11
	v_cvt_pk_f16_f32 v7, v12, v13
	v_cvt_pk_f16_f32 v8, v14, v15
	v_cvt_pk_f16_f32 v9, v16, v17
	v_xor_b32_e32 v72, 32, v70
	v_xor_b32_e32 v73, 0x2a0, v70
	ds_write_b128 v72, v[2:5]
	ds_write_b128 v73, v[6:9]
	ds_read_b64_tr_b16 v[206:207], v140
	ds_read_b64_tr_b16 v[208:209], v141
	ds_read_b64_tr_b16 v[210:211], v140 offset:32768
	ds_read_b64_tr_b16 v[212:213], v141 offset:32768
	s_waitcnt lgkmcnt(6)
	v_mfma_f32_32x32x16_f16 v[2:17], v[26:29], v[86:89], 0
	v_mfma_f32_32x32x16_f16 v[2:17], v[30:33], v[82:85], v[2:17]
	v_cvt_pk_f16_f32 v190, v190, v191
	v_cvt_pk_f16_f32 v191, v192, v193
	v_cvt_pk_f16_f32 v192, v194, v195
	v_cvt_pk_f16_f32 v193, v196, v197
	v_cvt_pk_f16_f32 v194, v198, v199
	v_cvt_pk_f16_f32 v195, v200, v201
	v_cvt_pk_f16_f32 v196, v202, v203
	v_cvt_pk_f16_f32 v197, v204, v205
	v_xor_b32_e32 v72, 48, v70
	v_xor_b32_e32 v73, 0x2b0, v70
	ds_write_b128 v72, v[190:193]
	ds_write_b128 v73, v[194:197]
	ds_read_b64_tr_b16 v[18:19], v138
	ds_read_b64_tr_b16 v[20:21], v139
	ds_read_b64_tr_b16 v[22:23], v138 offset:32768
	ds_read_b64_tr_b16 v[24:25], v139 offset:32768
	s_waitcnt lgkmcnt(6)
	v_mfma_f32_32x32x16_f16 v[190:205], v[206:209], v[86:89], 0
	v_mfma_f32_32x32x16_f16 v[190:205], v[210:213], v[82:85], v[190:205]
	v_cvt_pk_f16_f32 v2, v2, v3
	v_cvt_pk_f16_f32 v3, v4, v5
	v_cvt_pk_f16_f32 v4, v6, v7
	v_cvt_pk_f16_f32 v5, v8, v9
	v_cvt_pk_f16_f32 v6, v10, v11
	v_cvt_pk_f16_f32 v7, v12, v13
	v_cvt_pk_f16_f32 v8, v14, v15
	v_cvt_pk_f16_f32 v9, v16, v17
	v_xor_b32_e32 v72, 64, v70
	v_xor_b32_e32 v73, 0x2c0, v70
	ds_write_b128 v72, v[2:5]
	ds_write_b128 v73, v[6:9]
	ds_read_b64_tr_b16 v[26:27], v136
	ds_read_b64_tr_b16 v[28:29], v137
	ds_read_b64_tr_b16 v[30:31], v136 offset:32768
	ds_read_b64_tr_b16 v[32:33], v137 offset:32768
	s_waitcnt lgkmcnt(6)
	v_mfma_f32_32x32x16_f16 v[2:17], v[18:21], v[86:89], 0
	v_mfma_f32_32x32x16_f16 v[2:17], v[22:25], v[82:85], v[2:17]
	v_cvt_pk_f16_f32 v190, v190, v191
	v_cvt_pk_f16_f32 v191, v192, v193
	v_cvt_pk_f16_f32 v192, v194, v195
	v_cvt_pk_f16_f32 v193, v196, v197
	v_cvt_pk_f16_f32 v194, v198, v199
	v_cvt_pk_f16_f32 v195, v200, v201
	v_cvt_pk_f16_f32 v196, v202, v203
	v_cvt_pk_f16_f32 v197, v204, v205
	v_xor_b32_e32 v72, 0x50, v70
	v_xor_b32_e32 v73, 0x2d0, v70
	ds_write_b128 v72, v[190:193]
	ds_write_b128 v73, v[194:197]
	s_waitcnt lgkmcnt(2)
	v_mfma_f32_32x32x16_f16 v[190:205], v[26:29], v[86:89], 0
	v_mfma_f32_32x32x16_f16 v[190:205], v[30:33], v[82:85], v[190:205]
	v_cvt_pk_f16_f32 v2, v2, v3
	v_cvt_pk_f16_f32 v3, v4, v5
	v_cvt_pk_f16_f32 v4, v6, v7
	v_cvt_pk_f16_f32 v5, v8, v9
	v_cvt_pk_f16_f32 v6, v10, v11
	v_cvt_pk_f16_f32 v7, v12, v13
	v_cvt_pk_f16_f32 v8, v14, v15
	v_cvt_pk_f16_f32 v9, v16, v17
	v_xor_b32_e32 v72, 0x60, v70
	v_xor_b32_e32 v73, 0x2e0, v70
	ds_write_b128 v72, v[2:5]
	ds_write_b128 v73, v[6:9]
	v_cvt_pk_f16_f32 v190, v190, v191
	v_cvt_pk_f16_f32 v191, v192, v193
	v_cvt_pk_f16_f32 v192, v194, v195
	v_cvt_pk_f16_f32 v193, v196, v197
	v_cvt_pk_f16_f32 v194, v198, v199
	v_cvt_pk_f16_f32 v195, v200, v201
	v_cvt_pk_f16_f32 v196, v202, v203
	v_cvt_pk_f16_f32 v197, v204, v205
	v_xor_b32_e32 v72, 0x70, v70
	v_xor_b32_e32 v73, 0x2f0, v70
	ds_write_b128 v72, v[190:193]
	ds_write_b128 v73, v[194:197]
	v_lshl_add_u64 v[2:3], s[0:1], 0, v[154:155]
	v_lshl_add_u64 v[4:5], v[2:3], 0, s[18:19]
	v_add_co_u32_e32 v2, vcc, s25, v2
	s_waitcnt lgkmcnt(0)
	s_nop 0
	v_addc_co_u32_e32 v3, vcc, 0, v3, vcc
	s_barrier
	s_nop 0
	s_nop 0
	global_load_dwordx4 v[102:105], v[2:3], off
	global_load_dwordx4 v[98:101], v[4:5], off offset:1024
	s_setprio 1
	s_add_u32 s0, s2, 0x2000
	s_addc_u32 s1, s3, 0
	v_lshl_add_u64 v[2:3], s[0:1], 0, v[154:155]
	v_add_co_u32_e32 v2, vcc, s23, v2
	global_load_dwordx4 v[66:69], v154, s[0:1]
	global_load_dwordx4 v[70:73], v154, s[0:1] offset:1024
	global_load_dwordx4 v[74:77], v154, s[0:1] offset:2048
	global_load_dwordx4 v[78:81], v154, s[0:1] offset:3072
	v_addc_co_u32_e32 v3, vcc, 0, v3, vcc
	global_load_dwordx4 v[82:85], v168, s[0:1]
	global_load_dwordx4 v[86:89], v[2:3], off offset:1024
	global_load_dwordx4 v[182:185], v[2:3], off offset:2048
	global_load_dwordx4 v[186:189], v[2:3], off offset:3072
	ds_read_b128 v[18:21], v179
	ds_read_b128 v[22:25], v179 offset:32768
	ds_read_b128 v[26:29], v178
	ds_read_b128 v[30:33], v178 offset:32768
	s_add_u32 s0, s2, 0x6000
	s_addc_u32 s1, s3, 0
	s_waitcnt vmcnt(25) lgkmcnt(3)
	v_mfma_f32_32x32x16_f16 v[2:17], v[18:21], v[62:65], 0
	s_add_u32 s2, s2, 0x4000
	s_addc_u32 s3, s3, 0
	s_or_b32 s27, s26, 0x8a0
	s_or_b32 s26, s26, 0xa20
	s_waitcnt vmcnt(24) lgkmcnt(1)
	v_mfma_f32_32x32x16_f16 v[2:17], v[26:29], v[46:49], v[2:17]
	s_waitcnt vmcnt(23)
	v_mfma_f32_32x32x16_f16 v[2:17], v[22:25], v[42:45], v[2:17]
	s_waitcnt vmcnt(22) lgkmcnt(0)
	v_mfma_f32_32x32x16_f16 v[2:17], v[30:33], v[38:41], v[2:17]
	s_waitcnt vmcnt(15)
	v_mfma_f32_32x32x16_f16 v[34:49], v[18:21], v[34:37], 0
	s_nop 9
	v_cvt_pk_f16_f32 v9, v8, v9
	v_cvt_pk_f16_f32 v8, v6, v7
	v_cvt_pk_f16_f32 v7, v4, v5
	v_cvt_pk_f16_f32 v6, v2, v3
	v_cvt_pk_f16_f32 v5, v16, v17
	v_cvt_pk_f16_f32 v4, v14, v15
	v_cvt_pk_f16_f32 v3, v12, v13
	v_mfma_f32_32x32x16_f16 v[34:49], v[26:29], v[54:57], v[34:49]
	v_cvt_pk_f16_f32 v2, v10, v11
	v_mfma_f32_32x32x16_f16 v[34:49], v[22:25], v[50:53], v[34:49]
	s_waitcnt vmcnt(13)
	v_mfma_f32_32x32x16_f16 v[34:49], v[30:33], v[58:61], v[34:49]
	v_mfma_f32_32x32x16_f16 v[18:33], v[6:9], v[126:129], 0
	s_nop 10
	v_cvt_pk_f16_f32 v13, v40, v41
	v_cvt_pk_f16_f32 v12, v38, v39
	v_cvt_pk_f16_f32 v11, v36, v37
	v_cvt_pk_f16_f32 v10, v34, v35
	v_cvt_pk_f16_f32 v17, v48, v49
	v_cvt_pk_f16_f32 v16, v46, v47
	v_cvt_pk_f16_f32 v15, v44, v45
	v_mfma_f32_32x32x16_f16 v[50:65], v[6:9], v[110:113], 0
	v_bitop3_b32 v6, v171, s27, v170 bitop3:0x36
	v_cvt_pk_f16_f32 v14, v42, v43
	v_mfma_f32_32x32x16_f16 v[18:33], v[2:5], v[122:125], v[18:33]
	s_waitcnt vmcnt(12)
	v_mfma_f32_32x32x16_f16 v[50:65], v[2:5], v[106:109], v[50:65]
	ds_read_b128 v[2:5], v6
	ds_read_b128 v[6:9], v6 offset:32768
	v_mfma_f32_32x32x16_f16 v[18:33], v[10:13], v[118:121], v[18:33]
	s_waitcnt vmcnt(11)
	v_mfma_f32_32x32x16_f16 v[50:65], v[10:13], v[94:97], v[50:65]
	s_waitcnt vmcnt(7) lgkmcnt(1)
	v_mfma_f32_32x32x16_f16 v[34:49], v[2:5], v[66:69], 0
	v_mfma_f32_32x32x16_f16 v[18:33], v[14:17], v[114:117], v[18:33]
	v_mfma_f32_32x32x16_f16 v[50:65], v[14:17], v[90:93], v[50:65]
	v_bitop3_b32 v14, v171, s26, v170 bitop3:0x36
	ds_read_b128 v[10:13], v14
	ds_read_b128 v[14:17], v14 offset:32768
	s_nop 7
	v_cvt_pk_f16_f32 v25, v24, v25
	v_cvt_pk_f16_f32 v24, v22, v23
	v_cvt_pk_f16_f32 v23, v20, v21
	v_cvt_pk_f16_f32 v22, v18, v19
	v_cvt_pk_f16_f32 v21, v32, v33
	s_waitcnt vmcnt(6) lgkmcnt(1)
	v_mfma_f32_32x32x16_f16 v[34:49], v[10:13], v[70:73], v[34:49]
	v_cvt_pk_f16_f32 v20, v30, v31
	v_cvt_pk_f16_f32 v19, v28, v29
	v_cvt_pk_f16_f32 v18, v26, v27
	ds_write_b128 v173, v[22:25]
	ds_write_b128 v172, v[18:21]
	v_cvt_pk_f16_f32 v21, v56, v57
	v_cvt_pk_f16_f32 v20, v54, v55
	s_waitcnt vmcnt(5)
	v_mfma_f32_32x32x16_f16 v[34:49], v[6:9], v[74:77], v[34:49]
	v_cvt_pk_f16_f32 v19, v52, v53
	v_cvt_pk_f16_f32 v18, v50, v51
	ds_write_b128 v173, v[18:21] offset:32768
	v_cvt_pk_f16_f32 v21, v64, v65
	v_cvt_pk_f16_f32 v20, v62, v63
	v_cvt_pk_f16_f32 v19, v60, v61
	v_cvt_pk_f16_f32 v18, v58, v59
	s_waitcnt vmcnt(4) lgkmcnt(3)
	v_mfma_f32_32x32x16_f16 v[34:49], v[14:17], v[78:81], v[34:49]
	ds_write_b128 v172, v[18:21] offset:32768
	s_waitcnt vmcnt(3)
	v_mfma_f32_32x32x16_f16 v[66:81], v[2:5], v[82:85], 0
	s_nop 8
	v_cvt_pk_f16_f32 v41, v40, v41
	v_cvt_pk_f16_f32 v40, v38, v39
	v_cvt_pk_f16_f32 v39, v36, v37
	v_cvt_pk_f16_f32 v38, v34, v35
	v_cvt_pk_f16_f32 v85, v48, v49
	v_cvt_pk_f16_f32 v84, v46, v47
	v_cvt_pk_f16_f32 v83, v44, v45
	s_waitcnt vmcnt(2)
	v_mfma_f32_32x32x16_f16 v[66:81], v[10:13], v[86:89], v[66:81]
	v_cvt_pk_f16_f32 v82, v42, v43
	s_waitcnt vmcnt(1)
	v_mfma_f32_32x32x16_f16 v[66:81], v[6:9], v[182:185], v[66:81]
	s_waitcnt vmcnt(0)
	v_mfma_f32_32x32x16_f16 v[66:81], v[14:17], v[186:189], v[66:81]
	v_mfma_f32_32x32x16_f16 v[2:17], v[38:41], v[126:129], 0
	s_nop 10
	v_cvt_pk_f16_f32 v73, v72, v73
	v_cvt_pk_f16_f32 v72, v70, v71
	v_cvt_pk_f16_f32 v70, v66, v67
	v_cvt_pk_f16_f32 v67, v76, v77
	v_cvt_pk_f16_f32 v66, v74, v75
	global_load_dwordx4 v[74:77], v154, s[2:3]
	v_cvt_pk_f16_f32 v71, v68, v69
	v_cvt_pk_f16_f32 v69, v80, v81
	v_cvt_pk_f16_f32 v68, v78, v79
	global_load_dwordx4 v[78:81], v154, s[2:3] offset:1024
	ds_read_b128 v[18:21], v180
	ds_read_b128 v[22:25], v176
	ds_read_b128 v[26:29], v180 offset:32768
	global_load_dwordx4 v[30:33], v154, s[2:3] offset:2048
	v_mfma_f32_32x32x16_f16 v[34:49], v[38:41], v[110:113], 0
	v_mfma_f32_32x32x16_f16 v[2:17], v[82:85], v[122:125], v[2:17]
	v_mfma_f32_32x32x16_f16 v[34:49], v[82:85], v[106:109], v[34:49]
	ds_read_b128 v[82:85], v176 offset:32768
	s_waitcnt vmcnt(2) lgkmcnt(3)
	v_mfma_f32_32x32x16_f16 v[50:65], v[18:21], v[74:77], 0
	v_mfma_f32_32x32x16_f16 v[2:17], v[70:73], v[118:121], v[2:17]
	v_mfma_f32_32x32x16_f16 v[34:49], v[70:73], v[94:97], v[34:49]
	v_lshl_add_u64 v[70:71], s[2:3], 0, v[154:155]
	v_add_co_u32_e32 v152, vcc, s23, v70
	s_nop 1
	v_addc_co_u32_e32 v153, vcc, 0, v71, vcc
	s_waitcnt vmcnt(1) lgkmcnt(2)
	v_mfma_f32_32x32x16_f16 v[50:65], v[22:25], v[78:81], v[50:65]
	v_mfma_f32_32x32x16_f16 v[2:17], v[66:69], v[114:117], v[2:17]
	v_mfma_f32_32x32x16_f16 v[34:49], v[66:69], v[90:93], v[34:49]
	global_load_dwordx4 v[66:69], v154, s[2:3] offset:3072
	s_nop 9
	v_cvt_pk_f16_f32 v9, v8, v9
	v_cvt_pk_f16_f32 v8, v6, v7
	v_cvt_pk_f16_f32 v7, v4, v5
	v_cvt_pk_f16_f32 v6, v2, v3
	v_cvt_pk_f16_f32 v5, v16, v17
	v_cvt_pk_f16_f32 v4, v14, v15
	s_waitcnt vmcnt(1) lgkmcnt(1)
	v_mfma_f32_32x32x16_f16 v[50:65], v[26:29], v[30:33], v[50:65]
	global_load_dwordx4 v[30:33], v168, s[2:3]
	global_load_dwordx4 v[86:89], v[152:153], off offset:1024
	s_nop 0
	global_load_dwordx4 v[168:171], v168, s[0:1]
	v_cvt_pk_f16_f32 v3, v12, v13
	v_cvt_pk_f16_f32 v2, v10, v11
	ds_write_b128 v175, v[6:9]
	ds_write_b128 v174, v[2:5]
	v_cvt_pk_f16_f32 v5, v40, v41
	s_waitcnt vmcnt(3) lgkmcnt(2)
	v_mfma_f32_32x32x16_f16 v[50:65], v[82:85], v[66:69], v[50:65]
	global_load_dwordx4 v[182:185], v154, s[0:1] offset:1024
	v_cvt_pk_f16_f32 v4, v38, v39
	v_cvt_pk_f16_f32 v3, v36, v37
	v_cvt_pk_f16_f32 v2, v34, v35
	ds_write_b128 v175, v[2:5] offset:32768
	v_cvt_pk_f16_f32 v5, v48, v49
	v_cvt_pk_f16_f32 v4, v46, v47
	s_waitcnt vmcnt(3)
	v_mfma_f32_32x32x16_f16 v[66:81], v[18:21], v[30:33], 0
	global_load_dwordx4 v[18:21], v[152:153], off offset:2048
	v_cvt_pk_f16_f32 v3, v44, v45
	v_cvt_pk_f16_f32 v2, v42, v43
	ds_write_b128 v174, v[2:5] offset:32768
	v_cvt_pk_f16_f32 v57, v56, v57
	v_cvt_pk_f16_f32 v56, v54, v55
	v_cvt_pk_f16_f32 v55, v52, v53
	s_waitcnt vmcnt(3)
	v_mfma_f32_32x32x16_f16 v[66:81], v[22:25], v[86:89], v[66:81]
	global_load_dwordx4 v[22:25], v[152:153], off offset:3072
	v_cvt_pk_f16_f32 v54, v50, v51
	s_waitcnt vmcnt(1)
	v_mfma_f32_32x32x16_f16 v[66:81], v[26:29], v[18:21], v[66:81]
	v_lshl_add_u64 v[18:19], s[0:1], 0, v[154:155]
	v_add_co_u32_e32 v152, vcc, s23, v18
	s_nop 1
	v_addc_co_u32_e32 v153, vcc, 0, v19, vcc
	global_load_dwordx4 v[86:89], v[152:153], off offset:1024
	s_waitcnt vmcnt(1)
	v_mfma_f32_32x32x16_f16 v[66:81], v[82:85], v[22:25], v[66:81]
	v_cvt_pk_f16_f32 v85, v64, v65
	v_cvt_pk_f16_f32 v84, v62, v63
	v_cvt_pk_f16_f32 v83, v60, v61
	v_cvt_pk_f16_f32 v82, v58, v59
	v_mfma_f32_32x32x16_f16 v[18:33], v[54:57], v[126:129], 0
	s_nop 6
	v_cvt_pk_f16_f32 v73, v72, v73
	v_cvt_pk_f16_f32 v72, v70, v71
	v_cvt_pk_f16_f32 v70, v66, v67
	v_cvt_pk_f16_f32 v67, v76, v77
	v_cvt_pk_f16_f32 v66, v74, v75
	global_load_dwordx4 v[74:77], v154, s[0:1]
	ds_read_b128 v[2:5], v181
	ds_read_b128 v[6:9], v177
	ds_read_b128 v[10:13], v181 offset:32768
	global_load_dwordx4 v[14:17], v154, s[0:1] offset:2048
	global_load_dwordx4 v[34:37], v154, s[0:1] offset:3072
	v_mfma_f32_32x32x16_f16 v[50:65], v[54:57], v[110:113], 0
	v_cvt_pk_f16_f32 v71, v68, v69
	v_cvt_pk_f16_f32 v69, v80, v81
	v_cvt_pk_f16_f32 v68, v78, v79
	v_mfma_f32_32x32x16_f16 v[18:33], v[82:85], v[122:125], v[18:33]
	v_mfma_f32_32x32x16_f16 v[50:65], v[82:85], v[106:109], v[50:65]
	ds_read_b128 v[82:85], v177 offset:32768
	v_mfma_f32_32x32x16_f16 v[18:33], v[70:73], v[118:121], v[18:33]
	v_mfma_f32_32x32x16_f16 v[50:65], v[70:73], v[94:97], v[50:65]
	v_mfma_f32_32x32x16_f16 v[18:33], v[66:69], v[114:117], v[18:33]
	v_mfma_f32_32x32x16_f16 v[50:65], v[66:69], v[90:93], v[50:65]
	s_nop 10
	v_cvt_pk_f16_f32 v25, v24, v25
	v_cvt_pk_f16_f32 v24, v22, v23
	v_cvt_pk_f16_f32 v23, v20, v21
	v_cvt_pk_f16_f32 v22, v18, v19
	ds_write_b128 v132, v[22:25]
	s_waitcnt vmcnt(2) lgkmcnt(4)
	v_mfma_f32_32x32x16_f16 v[66:81], v[2:5], v[74:77], 0
	s_waitcnt lgkmcnt(3)
	v_mfma_f32_32x32x16_f16 v[66:81], v[6:9], v[182:185], v[66:81]
	s_waitcnt vmcnt(1) lgkmcnt(2)
	v_mfma_f32_32x32x16_f16 v[66:81], v[10:13], v[14:17], v[66:81]
	s_waitcnt vmcnt(0) lgkmcnt(1)
	v_mfma_f32_32x32x16_f16 v[66:81], v[82:85], v[34:37], v[66:81]
	v_mfma_f32_32x32x16_f16 v[34:49], v[2:5], v[168:171], 0
	global_load_dwordx4 v[2:5], v[152:153], off offset:2048
	s_nop 9
	v_cvt_pk_f16_f32 v73, v72, v73
	v_cvt_pk_f16_f32 v72, v70, v71
	v_cvt_pk_f16_f32 v71, v68, v69
	v_cvt_pk_f16_f32 v70, v66, v67
	v_cvt_pk_f16_f32 v69, v80, v81
	v_cvt_pk_f16_f32 v68, v78, v79
	v_mfma_f32_32x32x16_f16 v[34:49], v[6:9], v[86:89], v[34:49]
	global_load_dwordx4 v[6:9], v[152:153], off offset:3072
	v_cvt_pk_f16_f32 v67, v76, v77
	v_cvt_pk_f16_f32 v66, v74, v75
	s_waitcnt vmcnt(1)
	v_mfma_f32_32x32x16_f16 v[34:49], v[10:13], v[2:5], v[34:49]
	s_waitcnt vmcnt(0)
	v_mfma_f32_32x32x16_f16 v[34:49], v[82:85], v[6:9], v[34:49]
	v_mfma_f32_32x32x16_f16 v[2:17], v[70:73], v[126:129], 0
	s_nop 10
	v_cvt_pk_f16_f32 v41, v40, v41
	v_cvt_pk_f16_f32 v40, v38, v39
	v_cvt_pk_f16_f32 v38, v34, v35
	v_cvt_pk_f16_f32 v35, v44, v45
	v_cvt_pk_f16_f32 v34, v42, v43
	v_cvt_pk_f16_f32 v45, v32, v33
	v_cvt_pk_f16_f32 v44, v30, v31
	v_cvt_pk_f16_f32 v43, v28, v29
	v_cvt_pk_f16_f32 v42, v26, v27
	v_mfma_f32_32x32x16_f16 v[18:33], v[70:73], v[110:113], 0
	v_cvt_pk_f16_f32 v39, v36, v37
	v_cvt_pk_f16_f32 v37, v48, v49
	v_cvt_pk_f16_f32 v36, v46, v47
	ds_write_b128 v131, v[42:45]
	v_cvt_pk_f16_f32 v45, v56, v57
	v_cvt_pk_f16_f32 v44, v54, v55
	v_cvt_pk_f16_f32 v43, v52, v53
	v_mfma_f32_32x32x16_f16 v[2:17], v[66:69], v[122:125], v[2:17]
	v_cvt_pk_f16_f32 v42, v50, v51
	ds_write_b128 v132, v[42:45] offset:32768
	v_cvt_pk_f16_f32 v45, v64, v65
	v_cvt_pk_f16_f32 v44, v62, v63
	v_cvt_pk_f16_f32 v43, v60, v61
	v_cvt_pk_f16_f32 v42, v58, v59
	ds_write_b128 v131, v[42:45] offset:32768
	v_mfma_f32_32x32x16_f16 v[18:33], v[66:69], v[106:109], v[18:33]
	v_mfma_f32_32x32x16_f16 v[2:17], v[38:41], v[118:121], v[2:17]
	v_mfma_f32_32x32x16_f16 v[18:33], v[38:41], v[94:97], v[18:33]
	v_mfma_f32_32x32x16_f16 v[2:17], v[34:37], v[114:117], v[2:17]
	v_mfma_f32_32x32x16_f16 v[18:33], v[34:37], v[90:93], v[18:33]
	s_nop 10
	v_cvt_pk_f16_f32 v9, v8, v9
	v_cvt_pk_f16_f32 v8, v6, v7
	v_cvt_pk_f16_f32 v7, v4, v5
	v_cvt_pk_f16_f32 v6, v2, v3
	v_cvt_pk_f16_f32 v5, v16, v17
	v_cvt_pk_f16_f32 v4, v14, v15
	v_cvt_pk_f16_f32 v3, v12, v13
	v_cvt_pk_f16_f32 v2, v10, v11
	ds_write_b128 v135, v[6:9]
	ds_write_b128 v133, v[2:5]
	v_cvt_pk_f16_f32 v5, v24, v25
	v_cvt_pk_f16_f32 v4, v22, v23
	v_cvt_pk_f16_f32 v3, v20, v21
	v_cvt_pk_f16_f32 v2, v18, v19
	ds_write_b128 v135, v[2:5] offset:32768
	v_cvt_pk_f16_f32 v5, v32, v33
	v_cvt_pk_f16_f32 v4, v30, v31
	v_cvt_pk_f16_f32 v3, v28, v29
	v_cvt_pk_f16_f32 v2, v26, v27
	ds_write_b128 v133, v[2:5] offset:32768
	s_setprio 0
	s_waitcnt lgkmcnt(0)
	s_barrier
	ds_read_b64_tr_b16 v[2:3], v146
	ds_read_b64_tr_b16 v[4:5], v147
	ds_read_b64_tr_b16 v[36:37], v147 offset:32768
	ds_read_b64_tr_b16 v[34:35], v146 offset:32768
	ds_read_b64_tr_b16 v[18:19], v150
	ds_read_b64_tr_b16 v[20:21], v151
	ds_read_b64_tr_b16 v[40:41], v151 offset:32768
	ds_read_b64_tr_b16 v[38:39], v150 offset:32768
	s_waitcnt lgkmcnt(6)
	v_mfma_f32_32x32x16_f16 v[2:17], v[2:5], v[102:105], 0
	ds_read_b64_tr_b16 v[42:43], v148
	ds_read_b64_tr_b16 v[44:45], v149
	ds_read_b64_tr_b16 v[48:49], v149 offset:32768
	ds_read_b64_tr_b16 v[46:47], v148 offset:32768
	v_cmp_gt_u32_e64 s[0:1], 32, v167
	s_cmp_eq_u32 s5, 0
	v_cmp_lt_i32_e64 s[2:3], v162, v163
	s_waitcnt lgkmcnt(6)
	v_mfma_f32_32x32x16_f16 v[18:33], v[18:21], v[102:105], 0
	v_mfma_f32_32x32x16_f16 v[2:17], v[34:37], v[98:101], v[2:17]
	s_waitcnt lgkmcnt(4)
	v_mfma_f32_32x32x16_f16 v[18:33], v[38:41], v[98:101], v[18:33]
	s_nop 9
	v_mul_f32_e64 v34, v16, v16
	v_mul_f32_e64 v35, v17, v17
	v_mul_f32_e64 v36, v12, v12
	v_mul_f32_e64 v37, v13, v13
	v_mul_f32_e64 v50, v8, v8
	v_mul_f32_e64 v51, v9, v9
	v_pk_mul_f32 v[52:53], v[4:5], v[4:5]
	v_pk_fma_f32 v[50:51], v[6:7], v[6:7], v[50:51]
	v_pk_fma_f32 v[52:53], v[2:3], v[2:3], v[52:53]
	v_pk_fma_f32 v[36:37], v[10:11], v[10:11], v[36:37]
	v_pk_fma_f32 v[34:35], v[14:15], v[14:15], v[34:35]
	v_pk_mul_f32 v[116:117], v[24:25], v[24:25]
	v_pk_mul_f32 v[118:119], v[20:21], v[20:21]
	v_pk_add_f32 v[50:51], v[52:53], v[50:51]
	v_pk_add_f32 v[34:35], v[36:37], v[34:35]
	v_pk_mul_f32 v[112:113], v[32:33], v[32:33]
	v_pk_mul_f32 v[114:115], v[28:29], v[28:29]
	v_pk_mul_f32 v[120:121], v[18:19], v[18:19]
	v_pk_fma_f32 v[18:19], v[18:19], v[18:19], v[118:119]
	v_pk_fma_f32 v[20:21], v[22:23], v[22:23], v[116:117]
	v_pk_add_f32 v[34:35], v[50:51], v[34:35]
	v_pk_mul_f32 v[106:107], v[22:23], v[22:23]
	v_pk_add_f32 v[18:19], v[18:19], v[20:21]
	v_pk_fma_f32 v[20:21], v[26:27], v[26:27], v[114:115]
	v_pk_fma_f32 v[22:23], v[30:31], v[30:31], v[112:113]
	v_add_f32_e32 v34, v34, v35
	v_pk_add_f32 v[20:21], v[20:21], v[22:23]
	v_add_f32_e32 v36, 0, v34
	v_pk_mul_f32 v[108:109], v[26:27], v[26:27]
	v_pk_mul_f32 v[110:111], v[30:31], v[30:31]
	v_pk_add_f32 v[34:35], v[18:19], v[20:21]
	s_waitcnt lgkmcnt(2)
	v_mfma_f32_32x32x16_f16 v[18:33], v[42:45], v[102:105], 0
	v_add_f32_e32 v34, v34, v35
	v_add_f32_e32 v54, v36, v34
	v_sub_f32_e32 v55, v36, v34
	ds_read_b64_tr_b16 v[34:35], v144
	ds_read_b64_tr_b16 v[36:37], v145
	ds_read_b64_tr_b16 v[52:53], v145 offset:32768
	ds_read_b64_tr_b16 v[50:51], v144 offset:32768
	v_pk_fma_f32 v[4:5], v[4:5], v[4:5], v[118:119]
	v_pk_fma_f32 v[16:17], v[16:17], v[16:17], v[112:113]
	v_pk_fma_f32 v[14:15], v[14:15], v[14:15], v[110:111]
	s_waitcnt lgkmcnt(4)
	v_mfma_f32_32x32x16_f16 v[18:33], v[46:49], v[98:101], v[18:33]
	v_fma_f32 v12, v12, v12, v114
	v_fma_f32 v13, v13, v13, v115
	v_fma_f32 v10, v10, v10, v108
	v_fma_f32 v11, v11, v11, v109
	v_fma_f32 v8, v8, v8, v116
	v_fma_f32 v9, v9, v9, v117
	v_pk_fma_f32 v[6:7], v[6:7], v[6:7], v[106:107]
	v_pk_fma_f32 v[2:3], v[2:3], v[2:3], v[120:121]
	s_nop 3
	v_pk_mul_f32 v[38:39], v[32:33], v[32:33]
	v_pk_mul_f32 v[40:41], v[28:29], v[28:29]
	v_pk_mul_f32 v[42:43], v[24:25], v[24:25]
	v_pk_mul_f32 v[44:45], v[20:21], v[20:21]
	v_pk_fma_f32 v[42:43], v[22:23], v[22:23], v[42:43]
	v_pk_fma_f32 v[44:45], v[18:19], v[18:19], v[44:45]
	v_pk_fma_f32 v[40:41], v[26:27], v[26:27], v[40:41]
	v_pk_fma_f32 v[38:39], v[30:31], v[30:31], v[38:39]
	v_pk_add_f32 v[42:43], v[44:45], v[42:43]
	v_pk_add_f32 v[38:39], v[40:41], v[38:39]
	v_pk_fma_f32 v[4:5], v[20:21], v[20:21], v[4:5]
	v_pk_add_f32 v[38:39], v[42:43], v[38:39]
	v_pk_fma_f32 v[6:7], v[22:23], v[22:23], v[6:7]
	v_add_f32_e32 v56, v38, v39
	s_waitcnt lgkmcnt(2)
	v_mfma_f32_32x32x16_f16 v[34:49], v[34:37], v[102:105], 0
	v_add_f32_e32 v70, v54, v56
	v_add_f32_e32 v71, v55, v56
	v_sub_f32_e32 v72, v54, v56
	ds_read_b64_tr_b16 v[54:55], v142
	ds_read_b64_tr_b16 v[56:57], v143
	ds_read_b64_tr_b16 v[68:69], v143 offset:32768
	ds_read_b64_tr_b16 v[66:67], v142 offset:32768
	v_pk_fma_f32 v[8:9], v[24:25], v[24:25], v[8:9]
	v_pk_fma_f32 v[10:11], v[26:27], v[26:27], v[10:11]
	v_pk_fma_f32 v[12:13], v[28:29], v[28:29], v[12:13]
	s_waitcnt lgkmcnt(4)
	v_mfma_f32_32x32x16_f16 v[34:49], v[50:53], v[98:101], v[34:49]
	v_fma_f32 v14, v30, v30, v14
	v_fma_f32 v15, v31, v31, v15
	v_fma_f32 v16, v32, v32, v16
	v_fma_f32 v17, v33, v33, v17
	v_fma_f32 v2, v18, v18, v2
	v_fma_f32 v3, v19, v19, v3
	s_nop 5
	v_pk_mul_f32 v[50:51], v[48:49], v[48:49]
	v_pk_mul_f32 v[52:53], v[44:45], v[44:45]
	v_pk_mul_f32 v[58:59], v[40:41], v[40:41]
	v_pk_mul_f32 v[60:61], v[36:37], v[36:37]
	v_pk_fma_f32 v[58:59], v[38:39], v[38:39], v[58:59]
	v_pk_fma_f32 v[60:61], v[34:35], v[34:35], v[60:61]
	v_pk_fma_f32 v[52:53], v[42:43], v[42:43], v[52:53]
	v_pk_fma_f32 v[50:51], v[46:47], v[46:47], v[50:51]
	v_pk_add_f32 v[58:59], v[60:61], v[58:59]
	v_pk_add_f32 v[50:51], v[52:53], v[50:51]
	v_pk_fma_f32 v[4:5], v[36:37], v[36:37], v[4:5]
	v_pk_add_f32 v[50:51], v[58:59], v[50:51]
	v_pk_fma_f32 v[16:17], v[48:49], v[48:49], v[16:17]
	v_add_f32_e32 v73, v50, v51
	s_waitcnt lgkmcnt(2)
	v_mfma_f32_32x32x16_f16 v[50:65], v[54:57], v[102:105], 0
	v_add_f32_e32 v86, v70, v73
	v_sub_f32_e32 v87, v71, v73
	v_sub_f32_e32 v88, v72, v73
	ds_read_b64_tr_b16 v[70:71], v140
	ds_read_b64_tr_b16 v[72:73], v141
	ds_read_b64_tr_b16 v[84:85], v141 offset:32768
	ds_read_b64_tr_b16 v[82:83], v140 offset:32768
	v_pk_fma_f32 v[14:15], v[46:47], v[46:47], v[14:15]
	v_pk_fma_f32 v[12:13], v[44:45], v[44:45], v[12:13]
	v_pk_fma_f32 v[10:11], v[42:43], v[42:43], v[10:11]
	s_waitcnt lgkmcnt(4)
	v_mfma_f32_32x32x16_f16 v[50:65], v[66:69], v[98:101], v[50:65]
	v_fma_f32 v8, v40, v40, v8
	v_fma_f32 v9, v41, v41, v9
	v_fma_f32 v6, v38, v38, v6
	v_fma_f32 v7, v39, v39, v7
	v_fma_f32 v2, v34, v34, v2
	v_fma_f32 v3, v35, v35, v3
	s_nop 5
	v_pk_mul_f32 v[66:67], v[64:65], v[64:65]
	v_pk_mul_f32 v[68:69], v[60:61], v[60:61]
	v_pk_mul_f32 v[74:75], v[56:57], v[56:57]
	v_pk_mul_f32 v[76:77], v[52:53], v[52:53]
	v_pk_fma_f32 v[74:75], v[54:55], v[54:55], v[74:75]
	v_pk_fma_f32 v[76:77], v[50:51], v[50:51], v[76:77]
	v_pk_fma_f32 v[68:69], v[58:59], v[58:59], v[68:69]
	v_pk_fma_f32 v[66:67], v[62:63], v[62:63], v[66:67]
	v_pk_add_f32 v[74:75], v[76:77], v[74:75]
	v_pk_add_f32 v[66:67], v[68:69], v[66:67]
	v_pk_fma_f32 v[4:5], v[52:53], v[52:53], v[4:5]
	v_pk_add_f32 v[66:67], v[74:75], v[66:67]
	v_pk_fma_f32 v[6:7], v[54:55], v[54:55], v[6:7]
	v_add_f32_e32 v89, v66, v67
	s_waitcnt lgkmcnt(2)
	v_mfma_f32_32x32x16_f16 v[66:81], v[70:73], v[102:105], 0
	v_add_f32_e32 v94, v86, v89
	v_add_f32_e32 v126, v87, v89
	v_add_f32_e32 v127, v88, v89
	v_sub_f32_e32 v128, v86, v89
	ds_read_b64_tr_b16 v[86:87], v138
	ds_read_b64_tr_b16 v[88:89], v139
	ds_read_b64_tr_b16 v[124:125], v139 offset:32768
	ds_read_b64_tr_b16 v[122:123], v138 offset:32768
	v_pk_fma_f32 v[8:9], v[56:57], v[56:57], v[8:9]
	v_pk_fma_f32 v[10:11], v[58:59], v[58:59], v[10:11]
	s_waitcnt lgkmcnt(4)
	v_mfma_f32_32x32x16_f16 v[66:81], v[82:85], v[98:101], v[66:81]
	v_fma_f32 v12, v60, v60, v12
	v_fma_f32 v13, v61, v61, v13
	v_fma_f32 v14, v62, v62, v14
	v_fma_f32 v15, v63, v63, v15
	v_fma_f32 v16, v64, v64, v16
	v_fma_f32 v17, v65, v65, v17
	v_pk_fma_f32 v[2:3], v[50:51], v[50:51], v[2:3]
	s_nop 4
	v_pk_mul_f32 v[82:83], v[80:81], v[80:81]
	v_pk_mul_f32 v[84:85], v[76:77], v[76:77]
	v_pk_mul_f32 v[90:91], v[72:73], v[72:73]
	v_pk_mul_f32 v[92:93], v[68:69], v[68:69]
	v_pk_fma_f32 v[90:91], v[70:71], v[70:71], v[90:91]
	v_pk_fma_f32 v[92:93], v[66:67], v[66:67], v[92:93]
	v_pk_fma_f32 v[84:85], v[74:75], v[74:75], v[84:85]
	v_pk_fma_f32 v[82:83], v[78:79], v[78:79], v[82:83]
	v_pk_add_f32 v[90:91], v[92:93], v[90:91]
	v_pk_add_f32 v[82:83], v[84:85], v[82:83]
	v_pk_fma_f32 v[4:5], v[68:69], v[68:69], v[4:5]
	v_pk_add_f32 v[82:83], v[90:91], v[82:83]
	v_pk_fma_f32 v[18:19], v[80:81], v[80:81], v[16:17]
	v_add_f32_e32 v129, v82, v83
	v_add_f32_e32 v131, v94, v129
	s_waitcnt lgkmcnt(2)
	v_mfma_f32_32x32x16_f16 v[82:97], v[86:89], v[102:105], 0
	v_sub_f32_e32 v135, v126, v129
	v_add_f32_e32 v142, v127, v129
	v_sub_f32_e32 v143, v128, v129
	ds_read_b64_tr_b16 v[126:127], v136
	ds_read_b64_tr_b16 v[128:129], v137
	ds_read_b64_tr_b16 v[138:139], v137 offset:32768
	ds_read_b64_tr_b16 v[136:137], v136 offset:32768
	v_pk_fma_f32 v[20:21], v[78:79], v[78:79], v[14:15]
	v_pk_fma_f32 v[22:23], v[76:77], v[76:77], v[12:13]
	v_pk_fma_f32 v[24:25], v[74:75], v[74:75], v[10:11]
	s_waitcnt lgkmcnt(4)
	v_mfma_f32_32x32x16_f16 v[82:97], v[122:125], v[98:101], v[82:97]
	v_fma_f32 v26, v72, v72, v8
	v_fma_f32 v27, v73, v73, v9
	v_fma_f32 v28, v70, v70, v6
	v_fma_f32 v29, v71, v71, v7
	v_fma_f32 v30, v66, v66, v2
	v_fma_f32 v31, v67, v67, v3
	s_nop 5
	v_pk_fma_f32 v[32:33], v[84:85], v[84:85], v[4:5]
	s_waitcnt lgkmcnt(2)
	v_mfma_f32_32x32x16_f16 v[2:17], v[126:129], v[102:105], 0
	v_fma_f32 v28, v86, v86, v28
	v_fma_f32 v29, v87, v87, v29
	v_fma_f32 v24, v90, v90, v24
	v_fma_f32 v25, v91, v91, v25
	v_fma_f32 v22, v92, v92, v22
	v_fma_f32 v23, v93, v93, v23
	v_pk_fma_f32 v[20:21], v[94:95], v[94:95], v[20:21]
	v_pk_fma_f32 v[18:19], v[96:97], v[96:97], v[18:19]
	v_pk_fma_f32 v[30:31], v[82:83], v[82:83], v[30:31]
	v_pk_fma_f32 v[26:27], v[88:89], v[88:89], v[26:27]
	s_waitcnt lgkmcnt(0)
	v_mfma_f32_32x32x16_f16 v[2:17], v[136:139], v[98:101], v[2:17]
	v_mul_f32_e64 v122, v96, v96
	v_mul_f32_e64 v123, v97, v97
	v_mul_f32_e64 v124, v92, v92
	v_mul_f32_e64 v125, v93, v93
	v_mul_f32_e64 v132, v88, v88
	v_mul_f32_e64 v133, v89, v89
	v_pk_mul_f32 v[140:141], v[84:85], v[84:85]
	v_pk_fma_f32 v[132:133], v[86:87], v[86:87], v[132:133]
	v_pk_fma_f32 v[140:141], v[82:83], v[82:83], v[140:141]
	v_pk_fma_f32 v[124:125], v[90:91], v[90:91], v[124:125]
	s_nop 1
	v_pk_mul_f32 v[38:39], v[8:9], v[8:9]
	v_pk_mul_f32 v[40:41], v[4:5], v[4:5]
	v_pk_mul_f32 v[34:35], v[16:17], v[16:17]
	v_pk_mul_f32 v[36:37], v[12:13], v[12:13]
	v_pk_fma_f32 v[16:17], v[16:17], v[16:17], v[18:19]
	v_pk_fma_f32 v[18:19], v[14:15], v[14:15], v[20:21]
	v_pk_fma_f32 v[12:13], v[12:13], v[12:13], v[22:23]
	v_pk_fma_f32 v[20:21], v[10:11], v[10:11], v[24:25]
	v_pk_fma_f32 v[22:23], v[6:7], v[6:7], v[28:29]
	v_pk_fma_f32 v[24:25], v[2:3], v[2:3], v[30:31]
	v_pk_fma_f32 v[2:3], v[2:3], v[2:3], v[40:41]
	v_pk_fma_f32 v[6:7], v[6:7], v[6:7], v[38:39]
	v_pk_fma_f32 v[4:5], v[4:5], v[4:5], v[32:33]
	v_pk_add_f32 v[2:3], v[2:3], v[6:7]
	v_pk_fma_f32 v[6:7], v[10:11], v[10:11], v[36:37]
	v_pk_fma_f32 v[10:11], v[14:15], v[14:15], v[34:35]
	v_pk_fma_f32 v[8:9], v[8:9], v[8:9], v[26:27]
	v_pk_add_f32 v[6:7], v[6:7], v[10:11]
	v_sub_f32_e32 v10, v24, v25
	v_add_f32_e32 v11, v25, v24
	v_add_f32_e32 v10, v4, v10
	v_sub_f32_e32 v14, v11, v4
	v_add_f32_e32 v4, v4, v11
	v_sub_f32_e32 v10, v10, v5
	v_sub_f32_e32 v11, v14, v5
	v_add_f32_e32 v4, v5, v4
	v_add_f32_e32 v5, v22, v10
	v_add_f32_e32 v10, v22, v11
	v_sub_f32_e32 v11, v4, v22
	v_add_f32_e32 v4, v22, v4
	v_sub_f32_e32 v5, v5, v23
	v_add_f32_e32 v10, v23, v10
	v_sub_f32_e32 v11, v11, v23
	v_add_f32_e32 v4, v23, v4
	v_add_f32_e32 v5, v8, v5
	v_sub_f32_e32 v10, v10, v8
	v_sub_f32_e32 v11, v11, v8
	v_add_f32_e32 v4, v8, v4
	v_sub_f32_e32 v5, v5, v9
	v_pk_fma_f32 v[122:123], v[94:95], v[94:95], v[122:123]
	v_sub_f32_e32 v8, v10, v9
	v_sub_f32_e32 v10, v11, v9
	v_add_f32_e32 v4, v9, v4
	v_add_f32_e32 v5, v20, v5
	v_pk_add_f32 v[132:133], v[140:141], v[132:133]
	v_pk_add_f32 v[122:123], v[124:125], v[122:123]
	v_add_f32_e32 v8, v20, v8
	v_add_f32_e32 v9, v20, v10
	v_sub_f32_e32 v4, v4, v20
	v_sub_f32_e32 v5, v5, v21
	v_pk_add_f32 v[122:123], v[132:133], v[122:123]
	v_add_f32_e32 v8, v21, v8
	v_add_f32_e32 v9, v21, v9
	v_sub_f32_e32 v4, v4, v21
	v_add_f32_e32 v5, v12, v5
	v_add_f32_e32 v122, v122, v123
	v_pk_add_f32 v[2:3], v[2:3], v[6:7]
	v_sub_f32_e32 v8, v8, v12
	v_add_f32_e32 v9, v12, v9
	v_sub_f32_e32 v4, v4, v12
	v_sub_f32_e32 v5, v5, v13
	v_add_f32_e32 v123, v131, v122
	v_add_f32_e32 v2, v2, v3
	v_sub_f32_e32 v8, v8, v13
	v_add_f32_e32 v9, v13, v9
	v_sub_f32_e32 v4, v4, v13
	v_add_f32_e32 v5, v18, v5
	v_add_f32_e32 v3, v123, v2
	v_add_f32_e32 v8, v18, v8
	v_sub_f32_e32 v9, v9, v18
	v_sub_f32_e32 v4, v4, v18
	v_sub_f32_e32 v5, v5, v19
	v_and_b32_e32 v10, 8, v156
	v_add_f32_e32 v8, v19, v8
	v_sub_f32_e32 v9, v9, v19
	v_sub_f32_e32 v4, v4, v19
	v_add_f32_e32 v5, v16, v5
	v_cmp_eq_u32_e32 vcc, 0, v10
	v_cndmask_b32_e64 v10, -v3, v3, s[0:1]
	s_cselect_b64 s[0:1], -1, 0
	s_bitcmp0_b32 s4, 7
	v_sub_f32_e32 v8, v8, v16
	v_sub_f32_e32 v9, v9, v16
	v_sub_f32_e32 v4, v4, v16
	v_sub_f32_e32 v5, v5, v17
	v_cndmask_b32_e64 v11, -v3, v3, s[0:1]
	s_cselect_b64 s[0:1], -1, 0
	v_and_b32_e32 v16, 32, v156
	v_sub_f32_e32 v8, v8, v17
	v_cndmask_b32_e64 v5, -v5, v5, vcc
	v_cndmask_b32_e64 v12, -v3, v3, s[0:1]
	v_cndmask_b32_e64 v18, v161, v162, s[2:3]
	v_cmp_eq_u32_e64 s[2:3], 0, v16
	v_lshlrev_b32_e32 v18, 2, v18
	v_cmp_eq_u32_e64 s[0:1], 0, v134
	v_cndmask_b32_e64 v16, v11, v5, s[2:3]
	v_cndmask_b32_e64 v5, v5, v11, s[2:3]
	v_cndmask_b32_e64 v11, v8, v12, s[2:3]
	ds_bpermute_b32 v11, v18, v11
	v_and_b32_e32 v14, 2, v156
	v_cndmask_b32_e64 v13, -v3, v3, s[0:1]
	v_cmp_eq_u32_e64 s[0:1], 0, v14
	v_cndmask_b32_e64 v8, v12, v8, s[2:3]
	v_add_f32_e32 v124, v135, v122
	v_cndmask_b32_e64 v14, -v3, v3, s[0:1]
	v_cmp_eq_u32_e64 s[0:1], 0, v130
	v_sub_f32_e32 v4, v4, v17
	s_waitcnt lgkmcnt(0)
	v_add_f32_e32 v8, v8, v11
	v_cndmask_b32_e64 v15, -v3, v3, s[0:1]
	v_cndmask_b32_e64 v11, v14, v10, s[2:3]
	v_cndmask_b32_e64 v10, v10, v14, s[2:3]
	v_sub_f32_e32 v6, v124, v2
	v_sub_f32_e32 v9, v9, v17
	v_cndmask_b32_e64 v3, -v3, v3, vcc
	ds_bpermute_b32 v10, v18, v10
	v_cndmask_b32_e64 v12, v4, v15, s[2:3]
	v_sub_f32_e32 v125, v142, v122
	v_cndmask_b32_e64 v19, v9, v13, s[2:3]
	v_cndmask_b32_e64 v9, v13, v9, s[2:3]
	ds_bpermute_b32 v12, v18, v12
	v_cndmask_b32_e64 v13, v6, v3, s[2:3]
	v_sub_f32_e32 v7, v125, v2
	v_bfe_i32 v17, v156, 5, 1
	ds_bpermute_b32 v5, v18, v5
	ds_bpermute_b32 v13, v18, v13
	v_sub_f32_e32 v122, v143, v122
	v_cndmask_b32_e64 v3, v3, v6, s[2:3]
	v_and_b32_e32 v6, v17, v7
	v_sub_f32_e32 v2, v122, v2
	ds_bpermute_b32 v19, v18, v19
	ds_bpermute_b32 v6, v18, v6
	s_waitcnt lgkmcnt(5)
	v_add_f32_e32 v10, v11, v10
	v_cndmask_b32_e64 v4, v15, v4, s[2:3]
	v_and_b32_e32 v11, v17, v2
	s_waitcnt lgkmcnt(4)
	v_add_f32_e32 v4, v4, v12
	ds_bpermute_b32 v11, v18, v11
	v_and_b32_e32 v12, 16, v156
	v_cmp_lt_i32_e64 s[4:5], v164, v163
	s_waitcnt lgkmcnt(4)
	v_add_f32_e32 v5, v16, v5
	s_waitcnt lgkmcnt(3)
	v_add_f32_e32 v3, v3, v13
	v_cndmask_b32_e64 v13, v161, v164, s[4:5]
	v_cmp_eq_u32_e64 s[4:5], 0, v12
	s_waitcnt lgkmcnt(2)
	v_add_f32_e32 v9, v9, v19
	v_lshlrev_b32_e32 v13, 2, v13
	v_cndmask_b32_e64 v12, v4, v5, s[4:5]
	v_cndmask_b32_e64 v4, v5, v4, s[4:5]
	v_cndmask_b32_e64 v5, 0, v7, s[2:3]
	s_waitcnt lgkmcnt(1)
	v_add_f32_e32 v5, v5, v6
	v_cndmask_b32_e64 v2, 0, v2, s[2:3]
	v_cndmask_b32_e64 v7, v9, v5, s[4:5]
	ds_bpermute_b32 v4, v13, v4
	s_waitcnt lgkmcnt(1)
	v_add_f32_e32 v2, v2, v11
	v_cndmask_b32_e64 v6, v3, v8, s[4:5]
	v_cndmask_b32_e64 v3, v8, v3, s[4:5]
	ds_bpermute_b32 v7, v13, v7
	ds_bpermute_b32 v3, v13, v3
	v_cndmask_b32_e64 v8, v10, v2, s[4:5]
	ds_bpermute_b32 v8, v13, v8
	v_cndmask_b32_e64 v5, v5, v9, s[4:5]
	s_waitcnt lgkmcnt(3)
	v_add_f32_e32 v4, v12, v4
	s_waitcnt lgkmcnt(2)
	v_add_f32_e32 v5, v5, v7
	s_waitcnt lgkmcnt(1)
	v_add_f32_e32 v3, v6, v3
	v_cndmask_b32_e64 v2, v2, v10, s[4:5]
	v_cndmask_b32_e32 v6, v5, v4, vcc
	v_cndmask_b32_e32 v4, v4, v5, vcc
	v_mov_b32_e32 v5, v155
	s_waitcnt lgkmcnt(0)
	v_add_f32_e32 v2, v2, v8
	v_mov_b32_dpp v5, v4 row_mirror row_mask:0xf bank_mask:0xf
	s_nop 1
	v_add_f32_dpp v4, v5, v6 row_half_mirror row_mask:0xf bank_mask:0xf bound_ctrl:1
	v_cndmask_b32_e32 v5, v2, v3, vcc
	v_cndmask_b32_e32 v2, v3, v2, vcc
	v_mov_b32_e32 v3, v155
	s_nop 1
	v_mov_b32_dpp v3, v2 row_mirror row_mask:0xf bank_mask:0xf
	s_nop 1
	v_add_f32_dpp v2, v3, v5 row_half_mirror row_mask:0xf bank_mask:0xf bound_ctrl:1
	v_cndmask_b32_e64 v3, v2, v4, s[0:1]
	v_cndmask_b32_e64 v2, v4, v2, s[0:1]
	v_mov_b32_e32 v4, v155
	s_nop 1
	v_mov_b32_dpp v4, v2 row_half_mirror row_mask:0xf bank_mask:0xf
	s_nop 1
	v_add_f32_dpp v2, v4, v3 quad_perm:[3,2,1,0] row_mask:0xf bank_mask:0xf bound_ctrl:1
	v_and_b32_e32 v4, 3, v156
	v_cmp_eq_u32_e32 vcc, 0, v4
	v_and_b32_e32 v4, 56, v156
	v_add_f32_dpp v2, v2, v2 quad_perm:[2,3,0,1] row_mask:0xf bank_mask:0xf bound_ctrl:1
	v_mov_b32_e32 v3, 0
	v_cmp_ne_u32_e64 s[0:1], 56, v4
	s_and_b64 s[2:3], vcc, s[0:1]
	v_mov_b32_dpp v3, v2 quad_perm:[1,0,3,2] row_mask:0xf bank_mask:0xf
	s_and_saveexec_b64 s[0:1], s[2:3]
	v_and_b32_e32 v4, 0xfc, v156
	v_add_f32_e32 v2, v2, v3
	v_or_b32_e32 v4, v165, v4
	ds_write_b32 v4, v2
	s_or_b64 exec, exec, s[0:1]
	v_cmp_gt_i32_e32 vcc, 14, v156
	s_waitcnt lgkmcnt(0)
	s_barrier
	s_and_saveexec_b64 s[0:1], vcc
	s_cbranch_execz .LBB1_2
	ds_read_b32 v2, v166
	ds_read_b32 v3, v166 offset:64
	ds_read_b32 v4, v166 offset:128
	ds_read_b32 v5, v166 offset:192
	s_waitcnt lgkmcnt(2)
	v_add_f32_e32 v2, v2, v3
	s_waitcnt lgkmcnt(1)
	v_add_f32_e32 v2, v2, v4
	s_waitcnt lgkmcnt(0)
	v_add_f32_e32 v2, v2, v5
	v_mul_f32_e32 v4, 0x39800000, v2
	v_lshl_add_u64 v[2:3], v[156:157], 2, s[14:15]
	global_store_dword v[2:3], v4, off
	s_branch .LBB1_2
